# baseline (speedup 1.0000x reference)
.LE_cdone1:
	s_waitcnt lgkmcnt(0)
	s_barrier
	v_mov_b32_e32 v252, 0x20800
	ds_read_b32 v200, v252
	ds_read_b32 v201, v252 offset:4
	ds_read_b32 v202, v252 offset:8
	s_waitcnt lgkmcnt(0)
	s_nop 1
	v_readfirstlane_b32 s31, v200
	v_readfirstlane_b32 s29, v201
	v_readfirstlane_b32 s30, v202
	s_nop 3
	s_barrier
	s_lshl_b32 s49, s29, 19
	s_lshl_b32 s64, s32, 13
	s_add_u32 s49, s49, s64
	s_mov_b32 s51, s64
	s_add_u32 s52, s51, 0x0
	s_add_u32 s53, s51, 0x1000
	s_add_u32 s54, s51, 0x8000
	s_add_u32 s55, s51, 0x9000
	s_add_u32 s56, s51, 0x10000
	s_add_u32 s57, s51, 0x11000
	s_add_u32 s58, s51, 0x18000
	s_add_u32 s59, s51, 0x19000
	s_lshl_b32 s64, s29, 8
	s_lshl_b32 s65, s30, 1
	s_add_u32 s64, s64, s65
	s_lshr_b32 s65, s32, 1
	s_add_u32 s64, s64, s65
	s_lshl_b32 s64, s64, 11
	s_and_b32 s65, s32, 1
	s_lshl_b32 s65, s65, 9
	s_add_u32 s50, s64, s65
	s_sub_u32 s60, s28, 1
	s_lshl_b32 s64, s30, 2
	s_add_u32 s64, s64, s32
	s_lshl_b32 s64, s64, 16
	s_add_u32 s44, s4, s64
	s_addc_u32 s45, s5, 0
	global_load_dwordx4 a[0:3], v192, s[44:45] offset:0
	global_load_dwordx4 a[4:7], v192, s[44:45] offset:1024
	global_load_dwordx4 a[8:11], v192, s[44:45] offset:2048
	global_load_dwordx4 a[12:15], v192, s[44:45] offset:3072
	s_add_u32 s44, s44, 0x1000
	s_addc_u32 s45, s45, 0
	global_load_dwordx4 a[16:19], v192, s[44:45] offset:0
	global_load_dwordx4 a[20:23], v192, s[44:45] offset:1024
	global_load_dwordx4 a[24:27], v192, s[44:45] offset:2048
	global_load_dwordx4 a[28:31], v192, s[44:45] offset:3072
	s_add_u32 s44, s44, 0x1000
	s_addc_u32 s45, s45, 0
	global_load_dwordx4 a[32:35], v192, s[44:45] offset:0
	global_load_dwordx4 a[36:39], v192, s[44:45] offset:1024
	global_load_dwordx4 a[40:43], v192, s[44:45] offset:2048
	global_load_dwordx4 a[44:47], v192, s[44:45] offset:3072
	s_add_u32 s44, s44, 0x1000
	s_addc_u32 s45, s45, 0
	global_load_dwordx4 a[48:51], v192, s[44:45] offset:0
	global_load_dwordx4 a[52:55], v192, s[44:45] offset:1024
	global_load_dwordx4 a[56:59], v192, s[44:45] offset:2048
	global_load_dwordx4 a[60:63], v192, s[44:45] offset:3072
	s_add_u32 s44, s44, 0x1000
	s_addc_u32 s45, s45, 0
	global_load_dwordx4 a[64:67], v192, s[44:45] offset:0
	global_load_dwordx4 a[68:71], v192, s[44:45] offset:1024
	global_load_dwordx4 a[72:75], v192, s[44:45] offset:2048
	global_load_dwordx4 a[76:79], v192, s[44:45] offset:3072
	s_add_u32 s44, s44, 0x1000
	s_addc_u32 s45, s45, 0
	global_load_dwordx4 a[80:83], v192, s[44:45] offset:0
	global_load_dwordx4 a[84:87], v192, s[44:45] offset:1024
	global_load_dwordx4 a[88:91], v192, s[44:45] offset:2048
	global_load_dwordx4 a[92:95], v192, s[44:45] offset:3072
	s_add_u32 s44, s44, 0x1000
	s_addc_u32 s45, s45, 0
	global_load_dwordx4 a[96:99], v192, s[44:45] offset:0
	global_load_dwordx4 a[100:103], v192, s[44:45] offset:1024
	global_load_dwordx4 a[104:107], v192, s[44:45] offset:2048
	global_load_dwordx4 a[108:111], v192, s[44:45] offset:3072
	s_add_u32 s44, s44, 0x1000
	s_addc_u32 s45, s45, 0
	global_load_dwordx4 a[112:115], v192, s[44:45] offset:0
	global_load_dwordx4 a[116:119], v192, s[44:45] offset:1024
	global_load_dwordx4 a[120:123], v192, s[44:45] offset:2048
	global_load_dwordx4 a[124:127], v192, s[44:45] offset:3072
	s_add_u32 s44, s44, 0x1000
	s_addc_u32 s45, s45, 0
	s_waitcnt vmcnt(16)
	global_load_dwordx4 a[128:131], v192, s[44:45] offset:0
	global_load_dwordx4 a[132:135], v192, s[44:45] offset:1024
	global_load_dwordx4 a[136:139], v192, s[44:45] offset:2048
	global_load_dwordx4 a[140:143], v192, s[44:45] offset:3072
	s_add_u32 s44, s44, 0x1000
	s_addc_u32 s45, s45, 0
	global_load_dwordx4 a[144:147], v192, s[44:45] offset:0
	global_load_dwordx4 a[148:151], v192, s[44:45] offset:1024
	global_load_dwordx4 a[152:155], v192, s[44:45] offset:2048
	global_load_dwordx4 a[156:159], v192, s[44:45] offset:3072
	s_add_u32 s44, s44, 0x1000
	s_addc_u32 s45, s45, 0
	global_load_dwordx4 a[160:163], v192, s[44:45] offset:0
	global_load_dwordx4 a[164:167], v192, s[44:45] offset:1024
	global_load_dwordx4 a[168:171], v192, s[44:45] offset:2048
	global_load_dwordx4 a[172:175], v192, s[44:45] offset:3072
	s_add_u32 s44, s44, 0x1000
	s_addc_u32 s45, s45, 0
	global_load_dwordx4 a[176:179], v192, s[44:45] offset:0
	global_load_dwordx4 a[180:183], v192, s[44:45] offset:1024
	global_load_dwordx4 a[184:187], v192, s[44:45] offset:2048
	global_load_dwordx4 a[188:191], v192, s[44:45] offset:3072
	s_add_u32 s44, s44, 0x1000
	s_addc_u32 s45, s45, 0
	global_load_dwordx4 a[192:195], v192, s[44:45] offset:0
	global_load_dwordx4 a[196:199], v192, s[44:45] offset:1024
	global_load_dwordx4 a[200:203], v192, s[44:45] offset:2048
	global_load_dwordx4 a[204:207], v192, s[44:45] offset:3072
	s_add_u32 s44, s44, 0x1000
	s_addc_u32 s45, s45, 0
	global_load_dwordx4 a[208:211], v192, s[44:45] offset:0
	global_load_dwordx4 a[212:215], v192, s[44:45] offset:1024
	global_load_dwordx4 a[216:219], v192, s[44:45] offset:2048
	global_load_dwordx4 a[220:223], v192, s[44:45] offset:3072
	s_add_u32 s44, s44, 0x1000
	s_addc_u32 s45, s45, 0
	global_load_dwordx4 a[224:227], v192, s[44:45] offset:0
	global_load_dwordx4 a[228:231], v192, s[44:45] offset:1024
	global_load_dwordx4 a[232:235], v192, s[44:45] offset:2048
	global_load_dwordx4 a[236:239], v192, s[44:45] offset:3072
	s_add_u32 s44, s44, 0x1000
	s_addc_u32 s45, s45, 0
	global_load_dwordx4 a[240:243], v192, s[44:45] offset:0
	global_load_dwordx4 a[244:247], v192, s[44:45] offset:1024
	global_load_dwordx4 a[248:251], v192, s[44:45] offset:2048
	global_load_dwordx4 a[252:255], v192, s[44:45] offset:3072
	s_add_u32 s44, s44, 0x1000
	s_addc_u32 s45, s45, 0
	v_mov_b32_e32 v128, 0
	v_mov_b32_e32 v129, 0
	v_mov_b32_e32 v130, 0
	v_mov_b32_e32 v131, 0
	v_mov_b32_e32 v132, 0
	v_mov_b32_e32 v133, 0
	v_mov_b32_e32 v134, 0
	v_mov_b32_e32 v135, 0
	v_mov_b32_e32 v136, 0
	v_mov_b32_e32 v137, 0
	v_mov_b32_e32 v138, 0
	v_mov_b32_e32 v139, 0
	v_mov_b32_e32 v140, 0
	v_mov_b32_e32 v141, 0
	v_mov_b32_e32 v142, 0
	v_mov_b32_e32 v143, 0
	v_mov_b32_e32 v144, 0
	v_mov_b32_e32 v145, 0
	v_mov_b32_e32 v146, 0
	v_mov_b32_e32 v147, 0
	v_mov_b32_e32 v148, 0
	v_mov_b32_e32 v149, 0
	v_mov_b32_e32 v150, 0
	v_mov_b32_e32 v151, 0
	v_mov_b32_e32 v152, 0
	v_mov_b32_e32 v153, 0
	v_mov_b32_e32 v154, 0
	v_mov_b32_e32 v155, 0
	v_mov_b32_e32 v156, 0
	v_mov_b32_e32 v157, 0
	v_mov_b32_e32 v158, 0
	v_mov_b32_e32 v159, 0
	s_lshl_b32 s64, s30, 5
	s_lshl_b32 s65, s32, 3
	s_add_u32 s64, s64, s65
	v_lshlrev_b32_e32 v255, 2, v254
	v_add_u32_e32 v255, s64, v255
	v_lshlrev_b32_e32 v249, 3, v253
	v_lshl_add_u32 v249, v254, 2, v249
	v_lshlrev_b32_e32 v250, 12, v253
	v_lshl_add_u32 v250, v254, 4, v250
	v_lshrrev_b32_e32 v200, 3, v253
	v_and_b32_e32 v201, 7, v253
	v_lshl_add_u32 v202, v200, 10, v201
	v_add_u32_e32 v202, s64, v202
	v_lshl_add_u32 v202, v202, 1, v254
	v_lshlrev_b32_e32 v202, 2, v202
	global_load_dword v248, v202, s[14:15]
	v_mov_b32_e32 v203, 0xbfb8aa3b
	v_mov_b32_e32 v204, 0xc038aa3b
	v_cmp_eq_u32_e32 vcc, 2, v200
	s_nop 1
	v_cndmask_b32_e32 v203, v203, v204, vcc
	v_lshlrev_b32_e32 v205, 2, v255
	v_add_u32_e32 v206, 0x0, v205
	global_load_dwordx4 v[232:235], v206, s[16:17]
	v_add_u32_e32 v206, 0x1000, v205
	global_load_dwordx4 v[236:239], v206, s[16:17]
	v_add_u32_e32 v206, 0x2000, v205
	global_load_dwordx4 v[240:243], v206, s[16:17]
	v_add_u32_e32 v206, 0x3000, v205
	global_load_dwordx4 v[244:247], v206, s[16:17]
	s_waitcnt vmcnt(0)
	v_mul_f32_e32 v248, v203, v248
	s_mov_b32 s65, 0xbfb8aa3b
	v_mul_f32_e32 v232, s65, v232
	v_mul_f32_e32 v233, s65, v233
	v_mul_f32_e32 v234, s65, v234
	v_mul_f32_e32 v235, s65, v235
	s_mov_b32 s65, 0xbfb8aa3b
	v_mul_f32_e32 v236, s65, v236
	v_mul_f32_e32 v237, s65, v237
	v_mul_f32_e32 v238, s65, v238
	v_mul_f32_e32 v239, s65, v239
	s_mov_b32 s65, 0xc038aa3b
	v_mul_f32_e32 v240, s65, v240
	v_mul_f32_e32 v241, s65, v241
	v_mul_f32_e32 v242, s65, v242
	v_mul_f32_e32 v243, s65, v243
	s_mov_b32 s65, 0xbfb8aa3b
	v_mul_f32_e32 v244, s65, v244
	v_mul_f32_e32 v245, s65, v245
	v_mul_f32_e32 v246, s65, v246
	v_mul_f32_e32 v247, s65, v247
	s_lshl_b32 s65, s29, 20
	s_lshl_b32 s66, s64, 2
	s_add_u32 s65, s65, s66
	s_add_u32 s62, s26, s65
	s_addc_u32 s63, s27, 0
	s_waitcnt vmcnt(0)
	s_mov_b32 s33, 0
	s_lshl_b32 s64, s33, 11
	s_lshl_b32 s65, s29, 8
	s_add_u32 s64, s64, s65
	s_lshl_b32 s64, s64, 3
	s_add_u32 s42, s12, s64
	s_addc_u32 s43, s13, 0
	global_load_dword v228, v249, s[42:43] offset:0
	global_load_dword v229, v249, s[42:43] offset:256
	s_waitcnt vmcnt(0)
	v_mfma_f32_32x32x2_f32 v[0:15], v248, v228, v[232:247]
	v_mfma_f32_32x32x2_f32 v[16:31], v248, v229, v[232:247]
	s_nop 15
	s_nop 3
	s_lshl_b32 s64, s33, 11
	s_lshl_b32 s65, s29, 8
	s_add_u32 s64, s64, s65
	s_add_u32 s64, s64, 64
	s_lshl_b32 s64, s64, 3
	s_add_u32 s42, s12, s64
	s_addc_u32 s43, s13, 0
	global_load_dword v228, v249, s[42:43] offset:0
	global_load_dword v229, v249, s[42:43] offset:256
	s_waitcnt vmcnt(0)
	v_mfma_f32_32x32x2_f32 v[32:47], v248, v228, v[232:247]
	v_mfma_f32_32x32x2_f32 v[48:63], v248, v229, v[232:247]
	s_nop 15
	s_nop 3
	s_lshl_b32 s64, s33, 11
	s_lshl_b32 s65, s29, 8
	s_add_u32 s64, s64, s65
	s_add_u32 s64, s64, 128
	s_lshl_b32 s64, s64, 3
	s_add_u32 s42, s12, s64
	s_addc_u32 s43, s13, 0
	global_load_dword v228, v249, s[42:43] offset:0
	global_load_dword v229, v249, s[42:43] offset:256
	s_waitcnt vmcnt(0)
	v_mfma_f32_32x32x2_f32 v[64:79], v248, v228, v[232:247]
	v_mfma_f32_32x32x2_f32 v[80:95], v248, v229, v[232:247]
	s_nop 15
	s_nop 3
	s_lshl_b32 s64, s33, 11
	s_lshl_b32 s65, s29, 8
	s_add_u32 s64, s64, s65
	s_add_u32 s64, s64, 192
	s_lshl_b32 s64, s64, 3
	s_add_u32 s42, s12, s64
	s_addc_u32 s43, s13, 0
	global_load_dword v228, v249, s[42:43] offset:0
	global_load_dword v229, v249, s[42:43] offset:256
	s_waitcnt vmcnt(0)
	v_mfma_f32_32x32x2_f32 v[96:111], v248, v228, v[232:247]
	v_mfma_f32_32x32x2_f32 v[112:127], v248, v229, v[232:247]
	s_nop 15
	s_nop 3
	s_waitcnt vmcnt(0)
	s_waitcnt lgkmcnt(0)
	s_lshl_b32 s64, s33, 3
	s_add_u32 s64, s64, s29
	s_lshl_b32 s64, s64, 5
	s_add_u32 s64, s64, s30
	s_lshl_b32 s64, s64, 2
	s_add_u32 s40, s8, s64
	s_addc_u32 s41, s9, 0
	s_and_b32 s64, s33, 1
	s_lshl_b32 s64, s64, 22
	s_add_u32 s64, s64, s50
	s_add_u32 s36, s6, s64
	s_addc_u32 s37, s7, 0
	v_exp_f32_e32 v200, v0
	v_exp_f32_e32 v201, v1
	v_exp_f32_e32 v202, v2
	v_exp_f32_e32 v203, v3
	v_exp_f32_e32 v204, v4
	v_exp_f32_e32 v205, v5
	v_exp_f32_e32 v206, v6
	v_exp_f32_e32 v207, v7
	v_exp_f32_e32 v208, v8
	v_exp_f32_e32 v209, v9
	v_exp_f32_e32 v210, v10
	v_exp_f32_e32 v211, v11
	v_exp_f32_e32 v212, v12
	v_exp_f32_e32 v213, v13
	v_exp_f32_e32 v214, v14
	v_exp_f32_e32 v215, v15
	v_add_f32_e32 v200, 1.0, v200
	v_add_f32_e32 v201, 1.0, v201
	v_add_f32_e32 v202, 1.0, v202
	v_add_f32_e32 v203, 1.0, v203
	v_add_f32_e32 v204, 1.0, v204
	v_add_f32_e32 v205, 1.0, v205
	v_add_f32_e32 v206, 1.0, v206
	v_add_f32_e32 v207, 1.0, v207
	v_add_f32_e32 v208, 1.0, v208
	v_add_f32_e32 v209, 1.0, v209
	v_add_f32_e32 v210, 1.0, v210
	v_add_f32_e32 v211, 1.0, v211
	v_add_f32_e32 v212, 1.0, v212
	v_add_f32_e32 v213, 1.0, v213
	v_add_f32_e32 v214, 1.0, v214
	v_add_f32_e32 v215, 1.0, v215
	v_rcp_f32_e32 v200, v200
	v_rcp_f32_e32 v201, v201
	v_rcp_f32_e32 v202, v202
	v_rcp_f32_e32 v203, v203
	v_rcp_f32_e32 v204, v204
	v_rcp_f32_e32 v205, v205
	v_rcp_f32_e32 v206, v206
	v_rcp_f32_e32 v207, v207
	v_rcp_f32_e32 v208, v208
	v_rcp_f32_e32 v209, v209
	v_rcp_f32_e32 v210, v210
	v_rcp_f32_e32 v211, v211
	v_rcp_f32_e32 v212, v212
	v_rcp_f32_e32 v213, v213
	v_rcp_f32_e32 v214, v214
	v_rcp_f32_e32 v215, v215
	v_fmamk_f32 v208, v208, 0xc0b8aa3b, v198
	v_fmamk_f32 v209, v209, 0xc0b8aa3b, v198
	v_fmamk_f32 v210, v210, 0xc0b8aa3b, v198
	v_fmamk_f32 v211, v211, 0xc0b8aa3b, v198
	v_mul_f32_e32 v204, v204, v128
	v_mul_f32_e32 v205, v205, v129
	v_mul_f32_e32 v206, v206, v130
	v_mul_f32_e32 v207, v207, v131
	v_fma_f32 v128, v200, v208, v204
	v_fma_f32 v129, v201, v209, v205
	v_fma_f32 v130, v202, v210, v206
	v_fma_f32 v131, v203, v211, v207
	v_exp_f32_e32 v200, v128
	v_exp_f32_e32 v201, v129
	v_exp_f32_e32 v202, v130
	v_exp_f32_e32 v203, v131
	v_add_f32_e32 v200, 1.0, v200
	v_add_f32_e32 v201, 1.0, v201
	v_add_f32_e32 v202, 1.0, v202
	v_add_f32_e32 v203, 1.0, v203
	v_rcp_f32_e32 v200, v200
	v_rcp_f32_e32 v201, v201
	v_rcp_f32_e32 v202, v202
	v_rcp_f32_e32 v203, v203
	v_fma_f32 v200, v200, 2.0, -1.0
	v_fma_f32 v201, v201, 2.0, -1.0
	v_fma_f32 v202, v202, 2.0, -1.0
	v_fma_f32 v203, v203, 2.0, -1.0
	v_mul_f32_e32 v216, v212, v200
	v_mul_f32_e32 v217, v213, v201
	v_mul_f32_e32 v218, v214, v202
	v_mul_f32_e32 v219, v215, v203
	v_cvt_pk_f16_f32 v220, v216, v217
	v_cvt_pk_f16_f32 v221, v218, v219
	v_exp_f32_e32 v200, v16
	v_exp_f32_e32 v201, v17
	v_exp_f32_e32 v202, v18
	v_exp_f32_e32 v203, v19
	v_exp_f32_e32 v204, v20
	v_exp_f32_e32 v205, v21
	v_exp_f32_e32 v206, v22
	v_exp_f32_e32 v207, v23
	v_exp_f32_e32 v208, v24
	v_exp_f32_e32 v209, v25
	v_exp_f32_e32 v210, v26
	v_exp_f32_e32 v211, v27
	v_exp_f32_e32 v212, v28
	v_exp_f32_e32 v213, v29
	v_exp_f32_e32 v214, v30
	v_exp_f32_e32 v215, v31
	v_add_f32_e32 v200, 1.0, v200
	v_add_f32_e32 v201, 1.0, v201
	v_add_f32_e32 v202, 1.0, v202
	v_add_f32_e32 v203, 1.0, v203
	v_add_f32_e32 v204, 1.0, v204
	v_add_f32_e32 v205, 1.0, v205
	v_add_f32_e32 v206, 1.0, v206
	v_add_f32_e32 v207, 1.0, v207
	v_add_f32_e32 v208, 1.0, v208
	v_add_f32_e32 v209, 1.0, v209
	v_add_f32_e32 v210, 1.0, v210
	v_add_f32_e32 v211, 1.0, v211
	v_add_f32_e32 v212, 1.0, v212
	v_add_f32_e32 v213, 1.0, v213
	v_add_f32_e32 v214, 1.0, v214
	v_add_f32_e32 v215, 1.0, v215
	v_rcp_f32_e32 v200, v200
	v_rcp_f32_e32 v201, v201
	v_rcp_f32_e32 v202, v202
	v_rcp_f32_e32 v203, v203
	v_rcp_f32_e32 v204, v204
	v_rcp_f32_e32 v205, v205
	v_rcp_f32_e32 v206, v206
	v_rcp_f32_e32 v207, v207
	v_rcp_f32_e32 v208, v208
	v_rcp_f32_e32 v209, v209
	v_rcp_f32_e32 v210, v210
	v_rcp_f32_e32 v211, v211
	v_rcp_f32_e32 v212, v212
	v_rcp_f32_e32 v213, v213
	v_rcp_f32_e32 v214, v214
	v_rcp_f32_e32 v215, v215
	v_fmamk_f32 v208, v208, 0xc0b8aa3b, v198
	v_fmamk_f32 v209, v209, 0xc0b8aa3b, v198
	v_fmamk_f32 v210, v210, 0xc0b8aa3b, v198
	v_fmamk_f32 v211, v211, 0xc0b8aa3b, v198
	v_mul_f32_e32 v204, v204, v132
	v_mul_f32_e32 v205, v205, v133
	v_mul_f32_e32 v206, v206, v134
	v_mul_f32_e32 v207, v207, v135
	v_fma_f32 v132, v200, v208, v204
	v_fma_f32 v133, v201, v209, v205
	v_fma_f32 v134, v202, v210, v206
	v_fma_f32 v135, v203, v211, v207
	v_exp_f32_e32 v200, v132
	v_exp_f32_e32 v201, v133
	v_exp_f32_e32 v202, v134
	v_exp_f32_e32 v203, v135
	v_add_f32_e32 v200, 1.0, v200
	v_add_f32_e32 v201, 1.0, v201
	v_add_f32_e32 v202, 1.0, v202
	v_add_f32_e32 v203, 1.0, v203
	v_rcp_f32_e32 v200, v200
	v_rcp_f32_e32 v201, v201
	v_rcp_f32_e32 v202, v202
	v_rcp_f32_e32 v203, v203
	v_fma_f32 v200, v200, 2.0, -1.0
	v_fma_f32 v201, v201, 2.0, -1.0
	v_fma_f32 v202, v202, 2.0, -1.0
	v_fma_f32 v203, v203, 2.0, -1.0
	v_mul_f32_e32 v216, v212, v200
	v_mul_f32_e32 v217, v213, v201
	v_mul_f32_e32 v218, v214, v202
	v_mul_f32_e32 v219, v215, v203
	v_cvt_pk_f16_f32 v222, v216, v217
	v_cvt_pk_f16_f32 v223, v218, v219
	s_nop 1
	v_permlane32_swap_b32_e32 v220, v222
	v_permlane32_swap_b32_e32 v221, v223
	s_cmp_eq_u32 s31, 0
	s_cbranch_scc1 .LE_slow4
	global_store_dwordx4 v195, v[220:223], s[36:37] offset:0
	s_branch .LE_join5

.LE_join15:
	s_mov_b32 s33, 1
	s_lshl_b32 s64, s33, 11
	s_lshl_b32 s65, s29, 8
	s_add_u32 s64, s64, s65
	s_lshl_b32 s64, s64, 3
	s_add_u32 s42, s12, s64
	s_addc_u32 s43, s13, 0
	global_load_dword v228, v249, s[42:43] offset:0
	global_load_dword v229, v249, s[42:43] offset:256
	s_waitcnt vmcnt(0)
	v_mfma_f32_32x32x2_f32 v[0:15], v248, v228, v[232:247]
	v_mfma_f32_32x32x2_f32 v[16:31], v248, v229, v[232:247]
	s_nop 15
	s_nop 3
	s_lshl_b32 s64, s33, 11
	s_lshl_b32 s65, s29, 8
	s_add_u32 s64, s64, s65
	s_add_u32 s64, s64, 64
	s_lshl_b32 s64, s64, 3
	s_add_u32 s42, s12, s64
	s_addc_u32 s43, s13, 0
	global_load_dword v228, v249, s[42:43] offset:0
	global_load_dword v229, v249, s[42:43] offset:256
	s_waitcnt vmcnt(0)
	v_mfma_f32_32x32x2_f32 v[32:47], v248, v228, v[232:247]
	v_mfma_f32_32x32x2_f32 v[48:63], v248, v229, v[232:247]
	s_nop 15
	s_nop 3
	s_waitcnt vmcnt(0)
	s_waitcnt lgkmcnt(0)
	s_cmp_ge_u32 s33, s28
	s_cbranch_scc1 .LE_end17
	s_sub_u32 s71, s33, 1
	s_and_b32 s64, s71, 1
	s_lshl_b32 s64, s64, 22
	s_add_u32 s64, s64, s49
	s_add_u32 s34, s6, s64
	s_addc_u32 s35, s7, 0
	s_lshl_b32 s64, s71, 3
	s_add_u32 s64, s64, s29
	s_lshl_b32 s64, s64, 7
	s_add_u32 s38, s8, s64
	s_addc_u32 s39, s9, 0

.LE_loop16:
	s_sub_u32 s71, s33, 1
	s_add_u32 s61, s33, 1
	s_min_u32 s61, s61, s60
	s_and_b32 s64, s71, 1
	s_lshl_b32 s64, s64, 22
	s_add_u32 s64, s64, s50
	s_add_u32 s64, s64, 0x60000
	s_add_u32 s36, s6, s64
	s_addc_u32 s37, s7, 0
	s_lshl_b32 s64, s71, 3
	s_add_u32 s64, s64, s29
	s_lshl_b32 s64, s64, 5
	s_add_u32 s64, s64, s30
	s_lshl_b32 s64, s64, 2
	s_add_u32 s40, s8, s64
	s_addc_u32 s41, s9, 0
	s_lshl_b32 s64, s33, 11
	s_lshl_b32 s65, s29, 8
	s_add_u32 s64, s64, s65
	s_add_u32 s64, s64, 128
	s_lshl_b32 s64, s64, 3
	s_add_u32 s42, s12, s64
	s_addc_u32 s43, s13, 0
	s_nop 3
	global_load_dword v228, v249, s[42:43] offset:0
	global_load_dword v229, v249, s[42:43] offset:256
	s_waitcnt lgkmcnt(4)
	v_mfma_f32_32x32x16_f16 v[0:15], a[0:3], v[160:163], v[0:15]
	ds_read_b128 v[160:163], v192 offset:8192
	v_exp_f32_e32 v200, v96
	v_mfma_f32_32x32x16_f16 v[16:31], a[0:3], v[164:167], v[16:31]
	ds_read_b128 v[164:167], v192 offset:9216
	s_lshl_b32 s64, s71, 3
	s_add_u32 s64, s64, s29
	s_lshl_b32 s64, s64, 7
	s_add_u32 s38, s8, s64
	s_addc_u32 s39, s9, 0
	global_load_dword v251, v196, s[38:39] sc1
	v_exp_f32_e32 v201, v97
	v_add_f32_e32 v200, 1.0, v200
	v_mfma_f32_32x32x16_f16 v[0:15], a[4:7], v[168:171], v[0:15]
	ds_read_b128 v[168:171], v192 offset:10240
	v_exp_f32_e32 v202, v98
	v_add_f32_e32 v201, 1.0, v201
	v_mfma_f32_32x32x16_f16 v[16:31], a[4:7], v[172:175], v[16:31]
	ds_read_b128 v[172:175], v192 offset:11264
	global_load_lds_dwordx4 v192, s[44:45] offset:1024 sc1
	v_exp_f32_e32 v203, v99
	v_add_f32_e32 v202, 1.0, v202
	s_waitcnt lgkmcnt(4)
	v_mfma_f32_32x32x16_f16 v[0:15], a[8:11], v[176:179], v[0:15]
	ds_read_b128 v[176:179], v192 offset:12288
	v_exp_f32_e32 v204, v100
	v_add_f32_e32 v203, 1.0, v203
	v_mfma_f32_32x32x16_f16 v[16:31], a[8:11], v[180:183], v[16:31]
	ds_read_b128 v[180:183], v192 offset:13312
	v_exp_f32_e32 v205, v101
	v_add_f32_e32 v204, 1.0, v204
	v_mfma_f32_32x32x16_f16 v[0:15], a[12:15], v[184:187], v[0:15]
	ds_read_b128 v[184:187], v192 offset:14336
	v_exp_f32_e32 v206, v102
	v_add_f32_e32 v205, 1.0, v205
	v_mfma_f32_32x32x16_f16 v[16:31], a[12:15], v[188:191], v[16:31]
	ds_read_b128 v[188:191], v192 offset:15360
	global_load_lds_dwordx4 v192, s[44:45] offset:2048 sc1
	v_exp_f32_e32 v207, v103
	v_add_f32_e32 v206, 1.0, v206
	s_waitcnt lgkmcnt(4)
	v_mfma_f32_32x32x16_f16 v[0:15], a[16:19], v[160:163], v[0:15]
	ds_read_b128 v[160:163], v192 offset:16384
	v_exp_f32_e32 v208, v104
	v_add_f32_e32 v207, 1.0, v207
	v_mfma_f32_32x32x16_f16 v[16:31], a[16:19], v[164:167], v[16:31]
	ds_read_b128 v[164:167], v192 offset:17408
	v_exp_f32_e32 v209, v105
	v_add_f32_e32 v208, 1.0, v208
	v_mfma_f32_32x32x16_f16 v[0:15], a[20:23], v[168:171], v[0:15]
	ds_read_b128 v[168:171], v192 offset:18432
	v_exp_f32_e32 v210, v106
	v_add_f32_e32 v209, 1.0, v209
	v_mfma_f32_32x32x16_f16 v[16:31], a[20:23], v[172:175], v[16:31]
	ds_read_b128 v[172:175], v192 offset:19456
	global_load_lds_dwordx4 v192, s[44:45] offset:3072 sc1
	v_exp_f32_e32 v211, v107
	v_add_f32_e32 v210, 1.0, v210
	s_waitcnt lgkmcnt(4)
	v_mfma_f32_32x32x16_f16 v[0:15], a[24:27], v[176:179], v[0:15]
	ds_read_b128 v[176:179], v192 offset:20480
	v_exp_f32_e32 v212, v108
	v_add_f32_e32 v211, 1.0, v211
	v_mfma_f32_32x32x16_f16 v[16:31], a[24:27], v[180:183], v[16:31]
	ds_read_b128 v[180:183], v192 offset:21504
	v_exp_f32_e32 v213, v109
	v_add_f32_e32 v212, 1.0, v212
	v_mfma_f32_32x32x16_f16 v[0:15], a[28:31], v[184:187], v[0:15]
	ds_read_b128 v[184:187], v192 offset:22528
	v_exp_f32_e32 v214, v110
	v_add_f32_e32 v213, 1.0, v213
	v_mfma_f32_32x32x16_f16 v[16:31], a[28:31], v[188:191], v[16:31]
	ds_read_b128 v[188:191], v192 offset:23552
	s_add_u32 s44, s34, 0x11000
	s_addc_u32 s45, s35, 0
	s_mov_b32 m0, s57
	s_nop 0
	global_load_lds_dwordx4 v192, s[44:45] sc1
	v_exp_f32_e32 v215, v111
	v_add_f32_e32 v214, 1.0, v214
	s_waitcnt lgkmcnt(4)
	v_mfma_f32_32x32x16_f16 v[0:15], a[32:35], v[160:163], v[0:15]
	ds_read_b128 v[160:163], v192 offset:24576
	v_add_f32_e32 v215, 1.0, v215
	v_rcp_f32_e32 v200, v200
	v_mfma_f32_32x32x16_f16 v[16:31], a[32:35], v[164:167], v[16:31]
	ds_read_b128 v[164:167], v192 offset:25600
	v_rcp_f32_e32 v201, v201
	v_mfma_f32_32x32x16_f16 v[0:15], a[36:39], v[168:171], v[0:15]
	ds_read_b128 v[168:171], v192 offset:26624
	v_rcp_f32_e32 v202, v202
	v_mfma_f32_32x32x16_f16 v[16:31], a[36:39], v[172:175], v[16:31]
	ds_read_b128 v[172:175], v192 offset:27648
	global_load_lds_dwordx4 v192, s[44:45] offset:1024 sc1
	v_rcp_f32_e32 v203, v203
	s_waitcnt lgkmcnt(4)
	v_mfma_f32_32x32x16_f16 v[0:15], a[40:43], v[176:179], v[0:15]
	ds_read_b128 v[176:179], v192 offset:28672
	v_rcp_f32_e32 v204, v204
	v_mfma_f32_32x32x16_f16 v[16:31], a[40:43], v[180:183], v[16:31]
	ds_read_b128 v[180:183], v192 offset:29696
	v_rcp_f32_e32 v205, v205
	v_mul_f32_e32 v204, v204, v152
	v_mfma_f32_32x32x16_f16 v[0:15], a[44:47], v[184:187], v[0:15]
	ds_read_b128 v[184:187], v192 offset:30720
	v_rcp_f32_e32 v206, v206
	v_mul_f32_e32 v205, v205, v153
	v_mfma_f32_32x32x16_f16 v[16:31], a[44:47], v[188:191], v[16:31]
	ds_read_b128 v[188:191], v192 offset:31744
	global_load_lds_dwordx4 v192, s[44:45] offset:2048 sc1
	v_rcp_f32_e32 v207, v207
	v_mul_f32_e32 v206, v206, v154
	s_waitcnt vmcnt(10)
	s_barrier
	s_waitcnt lgkmcnt(4)
	v_mfma_f32_32x32x16_f16 v[0:15], a[48:51], v[160:163], v[0:15]
	ds_read_b128 v[160:163], v192 offset:32768
	v_rcp_f32_e32 v208, v208
	v_mul_f32_e32 v207, v207, v155
	v_mfma_f32_32x32x16_f16 v[16:31], a[48:51], v[164:167], v[16:31]
	ds_read_b128 v[164:167], v192 offset:33792
	v_rcp_f32_e32 v209, v209
	v_fmamk_f32 v208, v208, 0xc0b8aa3b, v198
	v_mfma_f32_32x32x16_f16 v[0:15], a[52:55], v[168:171], v[0:15]
	ds_read_b128 v[168:171], v192 offset:34816
	v_rcp_f32_e32 v210, v210
	v_fmamk_f32 v209, v209, 0xc0b8aa3b, v198
	v_fma_f32 v152, v200, v208, v204
	v_mfma_f32_32x32x16_f16 v[16:31], a[52:55], v[172:175], v[16:31]
	ds_read_b128 v[172:175], v192 offset:35840
	global_load_lds_dwordx4 v192, s[44:45] offset:3072 sc1
	v_rcp_f32_e32 v211, v211
	v_fmamk_f32 v210, v210, 0xc0b8aa3b, v198
	v_fma_f32 v153, v201, v209, v205
	s_waitcnt lgkmcnt(4)
	v_mfma_f32_32x32x16_f16 v[0:15], a[56:59], v[176:179], v[0:15]
	ds_read_b128 v[176:179], v192 offset:36864
	v_rcp_f32_e32 v212, v212
	v_fmamk_f32 v211, v211, 0xc0b8aa3b, v198
	v_fma_f32 v154, v202, v210, v206
	v_mfma_f32_32x32x16_f16 v[16:31], a[56:59], v[180:183], v[16:31]
	ds_read_b128 v[180:183], v192 offset:37888
	v_rcp_f32_e32 v213, v213
	v_fma_f32 v155, v203, v211, v207
	v_mfma_f32_32x32x16_f16 v[0:15], a[60:63], v[184:187], v[0:15]
	ds_read_b128 v[184:187], v192 offset:38912
	v_rcp_f32_e32 v214, v214
	v_mfma_f32_32x32x16_f16 v[16:31], a[60:63], v[188:191], v[16:31]
	ds_read_b128 v[188:191], v192 offset:39936
	s_add_u32 s44, s34, 0x18000
	s_addc_u32 s45, s35, 0
	s_mov_b32 m0, s58
	s_nop 0
	global_load_lds_dwordx4 v192, s[44:45] sc1
	v_rcp_f32_e32 v215, v215
	s_waitcnt lgkmcnt(4)
	v_mfma_f32_32x32x16_f16 v[0:15], a[64:67], v[160:163], v[0:15]
	ds_read_b128 v[160:163], v192 offset:40960
	v_exp_f32_e32 v200, v152
	v_mfma_f32_32x32x16_f16 v[16:31], a[64:67], v[164:167], v[16:31]
	ds_read_b128 v[164:167], v192 offset:41984
	v_exp_f32_e32 v201, v153
	v_add_f32_e32 v200, 1.0, v200
	v_mfma_f32_32x32x16_f16 v[0:15], a[68:71], v[168:171], v[0:15]
	ds_read_b128 v[168:171], v192 offset:43008
	v_exp_f32_e32 v202, v154
	v_add_f32_e32 v201, 1.0, v201
	v_mfma_f32_32x32x16_f16 v[16:31], a[68:71], v[172:175], v[16:31]
	ds_read_b128 v[172:175], v192 offset:44032
	global_load_lds_dwordx4 v192, s[44:45] offset:1024 sc1
	v_exp_f32_e32 v203, v155
	v_add_f32_e32 v202, 1.0, v202
	s_waitcnt lgkmcnt(4)
	v_mfma_f32_32x32x16_f16 v[0:15], a[72:75], v[176:179], v[0:15]
	ds_read_b128 v[176:179], v192 offset:45056
	v_add_f32_e32 v203, 1.0, v203
	v_rcp_f32_e32 v200, v200
	v_mfma_f32_32x32x16_f16 v[16:31], a[72:75], v[180:183], v[16:31]
	ds_read_b128 v[180:183], v192 offset:46080
	v_rcp_f32_e32 v201, v201
	v_fma_f32 v200, v200, 2.0, -1.0
	v_mfma_f32_32x32x16_f16 v[0:15], a[76:79], v[184:187], v[0:15]
	ds_read_b128 v[184:187], v192 offset:47104
	v_rcp_f32_e32 v202, v202
	v_fma_f32 v201, v201, 2.0, -1.0
	v_mul_f32_e32 v216, v212, v200
	v_mfma_f32_32x32x16_f16 v[16:31], a[76:79], v[188:191], v[16:31]
	ds_read_b128 v[188:191], v192 offset:48128
	global_load_lds_dwordx4 v192, s[44:45] offset:2048 sc1
	v_rcp_f32_e32 v203, v203
	v_fma_f32 v202, v202, 2.0, -1.0
	v_mul_f32_e32 v217, v213, v201
	s_waitcnt lgkmcnt(4)
	v_mfma_f32_32x32x16_f16 v[0:15], a[80:83], v[160:163], v[0:15]
	ds_read_b128 v[160:163], v192 offset:49152
	v_fma_f32 v203, v203, 2.0, -1.0
	v_mul_f32_e32 v218, v214, v202
	v_exp_f32_e32 v200, v112
	v_mfma_f32_32x32x16_f16 v[16:31], a[80:83], v[164:167], v[16:31]
	ds_read_b128 v[164:167], v192 offset:50176
	v_mul_f32_e32 v219, v215, v203
	v_cvt_pk_f16_f32 v220, v216, v217
	v_exp_f32_e32 v201, v113
	v_mfma_f32_32x32x16_f16 v[0:15], a[84:87], v[168:171], v[0:15]
	ds_read_b128 v[168:171], v192 offset:51200
	v_cvt_pk_f16_f32 v221, v218, v219
	v_exp_f32_e32 v202, v114
	v_add_f32_e32 v200, 1.0, v200
	v_mfma_f32_32x32x16_f16 v[16:31], a[84:87], v[172:175], v[16:31]
	ds_read_b128 v[172:175], v192 offset:52224
	global_load_lds_dwordx4 v192, s[44:45] offset:3072 sc1
	v_exp_f32_e32 v203, v115
	v_add_f32_e32 v201, 1.0, v201
	v_add_f32_e32 v202, 1.0, v202
	s_waitcnt lgkmcnt(4)
	v_mfma_f32_32x32x16_f16 v[0:15], a[88:91], v[176:179], v[0:15]
	ds_read_b128 v[176:179], v192 offset:53248
	v_exp_f32_e32 v204, v116
	v_add_f32_e32 v203, 1.0, v203
	v_mfma_f32_32x32x16_f16 v[16:31], a[88:91], v[180:183], v[16:31]
	ds_read_b128 v[180:183], v192 offset:54272
	v_exp_f32_e32 v205, v117
	v_add_f32_e32 v204, 1.0, v204
	v_mfma_f32_32x32x16_f16 v[0:15], a[92:95], v[184:187], v[0:15]
	ds_read_b128 v[184:187], v192 offset:55296
	v_exp_f32_e32 v206, v118
	v_add_f32_e32 v205, 1.0, v205
	v_mfma_f32_32x32x16_f16 v[16:31], a[92:95], v[188:191], v[16:31]
	ds_read_b128 v[188:191], v192 offset:56320
	s_add_u32 s44, s34, 0x19000
	s_addc_u32 s45, s35, 0
	s_mov_b32 m0, s59
	s_nop 0
	global_load_lds_dwordx4 v192, s[44:45] sc1
	v_exp_f32_e32 v207, v119
	v_add_f32_e32 v206, 1.0, v206
	s_waitcnt lgkmcnt(4)
	v_mfma_f32_32x32x16_f16 v[0:15], a[96:99], v[160:163], v[0:15]
	ds_read_b128 v[160:163], v192 offset:57344
	v_exp_f32_e32 v208, v120
	v_add_f32_e32 v207, 1.0, v207
	v_mfma_f32_32x32x16_f16 v[16:31], a[96:99], v[164:167], v[16:31]
	ds_read_b128 v[164:167], v192 offset:58368
	v_exp_f32_e32 v209, v121
	v_add_f32_e32 v208, 1.0, v208
	v_mfma_f32_32x32x16_f16 v[0:15], a[100:103], v[168:171], v[0:15]
	ds_read_b128 v[168:171], v192 offset:59392
	v_exp_f32_e32 v210, v122
	v_add_f32_e32 v209, 1.0, v209
	v_mfma_f32_32x32x16_f16 v[16:31], a[100:103], v[172:175], v[16:31]
	ds_read_b128 v[172:175], v192 offset:60416
	global_load_lds_dwordx4 v192, s[44:45] offset:1024 sc1
	v_exp_f32_e32 v211, v123
	v_add_f32_e32 v210, 1.0, v210
	s_waitcnt lgkmcnt(4)
	v_mfma_f32_32x32x16_f16 v[0:15], a[104:107], v[176:179], v[0:15]
	ds_read_b128 v[176:179], v192 offset:61440
	v_exp_f32_e32 v212, v124
	v_add_f32_e32 v211, 1.0, v211
	v_mfma_f32_32x32x16_f16 v[16:31], a[104:107], v[180:183], v[16:31]
	ds_read_b128 v[180:183], v192 offset:62464
	v_exp_f32_e32 v213, v125
	v_add_f32_e32 v212, 1.0, v212
	v_mfma_f32_32x32x16_f16 v[0:15], a[108:111], v[184:187], v[0:15]
	ds_read_b128 v[184:187], v192 offset:63488
	v_exp_f32_e32 v214, v126
	v_add_f32_e32 v213, 1.0, v213
	v_mfma_f32_32x32x16_f16 v[16:31], a[108:111], v[188:191], v[16:31]
	ds_read_b128 v[188:191], v192 offset:64512
	global_load_lds_dwordx4 v192, s[44:45] offset:2048 sc1
	v_exp_f32_e32 v215, v127
	v_add_f32_e32 v214, 1.0, v214
	s_waitcnt vmcnt(7)
	s_barrier
	s_waitcnt lgkmcnt(4)
	v_mfma_f32_32x32x16_f16 v[0:15], a[112:115], v[160:163], v[0:15]
	ds_read_b128 v[160:163], v193 offset:0
	v_add_f32_e32 v215, 1.0, v215
	v_rcp_f32_e32 v200, v200
	v_mfma_f32_32x32x16_f16 v[16:31], a[112:115], v[164:167], v[16:31]
	ds_read_b128 v[164:167], v193 offset:1024
	v_rcp_f32_e32 v201, v201
	v_mfma_f32_32x32x16_f16 v[0:15], a[116:119], v[168:171], v[0:15]
	ds_read_b128 v[168:171], v193 offset:2048
	v_rcp_f32_e32 v202, v202
	v_mfma_f32_32x32x16_f16 v[16:31], a[116:119], v[172:175], v[16:31]
	ds_read_b128 v[172:175], v193 offset:3072
	global_load_lds_dwordx4 v192, s[44:45] offset:3072 sc1
	v_rcp_f32_e32 v203, v203
	s_waitcnt lgkmcnt(4)
	v_mfma_f32_32x32x16_f16 v[0:15], a[120:123], v[176:179], v[0:15]
	ds_read_b128 v[176:179], v193 offset:4096
	v_rcp_f32_e32 v204, v204
	v_mfma_f32_32x32x16_f16 v[16:31], a[120:123], v[180:183], v[16:31]
	ds_read_b128 v[180:183], v193 offset:5120
	v_rcp_f32_e32 v205, v205
	v_mul_f32_e32 v204, v204, v156
	v_mfma_f32_32x32x2_f32 v[64:79], v248, v228, v[232:247]
	v_mfma_f32_32x32x16_f16 v[0:15], a[124:127], v[184:187], v[0:15]
	ds_read_b128 v[184:187], v193 offset:6144
	v_rcp_f32_e32 v206, v206
	v_mul_f32_e32 v205, v205, v157
	v_mfma_f32_32x32x2_f32 v[80:95], v248, v229, v[232:247]
	v_mfma_f32_32x32x16_f16 v[16:31], a[124:127], v[188:191], v[16:31]
	ds_read_b128 v[188:191], v193 offset:7168
	v_cmp_gt_u32_e32 vcc, 2, v251
	s_cbranch_vccz .LE_tok20

.LE_tok20:
	s_and_b32 s64, s71, 1
	s_lshl_b32 s64, s64, 22
	s_add_u32 s64, s64, s49
	s_add_u32 s64, s64, 0x20000
	s_add_u32 s34, s6, s64
	s_addc_u32 s35, s7, 0
	s_add_u32 s44, s34, 0x0
	s_addc_u32 s45, s35, 0
	s_mov_b32 m0, s52
	s_nop 0
	global_load_lds_dwordx4 v192, s[44:45] sc1
	v_rcp_f32_e32 v207, v207
	v_mul_f32_e32 v206, v206, v158
	s_waitcnt lgkmcnt(4)
	v_mfma_f32_32x32x16_f16 v[0:15], a[128:131], v[160:163], v[0:15]
	ds_read_b128 v[160:163], v193 offset:8192
	v_rcp_f32_e32 v208, v208
	v_mul_f32_e32 v207, v207, v159
	v_mfma_f32_32x32x16_f16 v[16:31], a[128:131], v[164:167], v[16:31]
	ds_read_b128 v[164:167], v193 offset:9216
	v_rcp_f32_e32 v209, v209
	v_fmamk_f32 v208, v208, 0xc0b8aa3b, v198
	v_mfma_f32_32x32x16_f16 v[0:15], a[132:135], v[168:171], v[0:15]
	ds_read_b128 v[168:171], v193 offset:10240
	v_rcp_f32_e32 v210, v210
	v_fmamk_f32 v209, v209, 0xc0b8aa3b, v198
	v_fma_f32 v156, v200, v208, v204
	v_mfma_f32_32x32x16_f16 v[16:31], a[132:135], v[172:175], v[16:31]
	ds_read_b128 v[172:175], v193 offset:11264
	global_load_lds_dwordx4 v192, s[44:45] offset:1024 sc1
	v_rcp_f32_e32 v211, v211
	v_fmamk_f32 v210, v210, 0xc0b8aa3b, v198
	v_fma_f32 v157, v201, v209, v205
	s_waitcnt lgkmcnt(4)
	v_mfma_f32_32x32x16_f16 v[0:15], a[136:139], v[176:179], v[0:15]
	ds_read_b128 v[176:179], v193 offset:12288
	v_rcp_f32_e32 v212, v212
	v_fmamk_f32 v211, v211, 0xc0b8aa3b, v198
	v_fma_f32 v158, v202, v210, v206
	v_mfma_f32_32x32x16_f16 v[16:31], a[136:139], v[180:183], v[16:31]
	ds_read_b128 v[180:183], v193 offset:13312
	v_rcp_f32_e32 v213, v213
	v_fma_f32 v159, v203, v211, v207
	v_mfma_f32_32x32x16_f16 v[0:15], a[140:143], v[184:187], v[0:15]
	ds_read_b128 v[184:187], v193 offset:14336
	v_rcp_f32_e32 v214, v214
	v_mfma_f32_32x32x16_f16 v[16:31], a[140:143], v[188:191], v[16:31]
	ds_read_b128 v[188:191], v193 offset:15360
	global_load_lds_dwordx4 v192, s[44:45] offset:2048 sc1
	v_rcp_f32_e32 v215, v215
	s_waitcnt lgkmcnt(4)
	v_mfma_f32_32x32x16_f16 v[0:15], a[144:147], v[160:163], v[0:15]
	ds_read_b128 v[160:163], v193 offset:16384
	v_exp_f32_e32 v200, v156
	v_mfma_f32_32x32x16_f16 v[16:31], a[144:147], v[164:167], v[16:31]
	ds_read_b128 v[164:167], v193 offset:17408
	v_exp_f32_e32 v201, v157
	v_add_f32_e32 v200, 1.0, v200
	v_mfma_f32_32x32x16_f16 v[0:15], a[148:151], v[168:171], v[0:15]
	ds_read_b128 v[168:171], v193 offset:18432
	v_exp_f32_e32 v202, v158
	v_add_f32_e32 v201, 1.0, v201
	v_mfma_f32_32x32x16_f16 v[16:31], a[148:151], v[172:175], v[16:31]
	ds_read_b128 v[172:175], v193 offset:19456
	global_load_lds_dwordx4 v192, s[44:45] offset:3072 sc1
	v_exp_f32_e32 v203, v159
	v_add_f32_e32 v202, 1.0, v202
	s_waitcnt lgkmcnt(4)
	v_mfma_f32_32x32x16_f16 v[0:15], a[152:155], v[176:179], v[0:15]
	ds_read_b128 v[176:179], v193 offset:20480
	v_add_f32_e32 v203, 1.0, v203
	v_rcp_f32_e32 v200, v200
	v_mfma_f32_32x32x16_f16 v[16:31], a[152:155], v[180:183], v[16:31]
	ds_read_b128 v[180:183], v193 offset:21504
	v_rcp_f32_e32 v201, v201
	v_fma_f32 v200, v200, 2.0, -1.0
	v_mfma_f32_32x32x16_f16 v[0:15], a[156:159], v[184:187], v[0:15]
	ds_read_b128 v[184:187], v193 offset:22528
	v_rcp_f32_e32 v202, v202
	v_fma_f32 v201, v201, 2.0, -1.0
	v_mul_f32_e32 v216, v212, v200
	v_mfma_f32_32x32x16_f16 v[16:31], a[156:159], v[188:191], v[16:31]
	ds_read_b128 v[188:191], v193 offset:23552
	s_add_u32 s44, s34, 0x1000
	s_addc_u32 s45, s35, 0
	s_mov_b32 m0, s53
	s_nop 0
	global_load_lds_dwordx4 v192, s[44:45] sc1
	v_rcp_f32_e32 v203, v203
	v_fma_f32 v202, v202, 2.0, -1.0
	v_mul_f32_e32 v217, v213, v201
	s_waitcnt lgkmcnt(4)
	v_mfma_f32_32x32x16_f16 v[0:15], a[160:163], v[160:163], v[0:15]
	ds_read_b128 v[160:163], v193 offset:24576
	v_fma_f32 v203, v203, 2.0, -1.0
	v_mul_f32_e32 v218, v214, v202
	v_mfma_f32_32x32x16_f16 v[16:31], a[160:163], v[164:167], v[16:31]
	ds_read_b128 v[164:167], v193 offset:25600
	v_mul_f32_e32 v219, v215, v203
	v_cvt_pk_f16_f32 v222, v216, v217
	v_mfma_f32_32x32x16_f16 v[0:15], a[164:167], v[168:171], v[0:15]
	ds_read_b128 v[168:171], v193 offset:26624
	v_cvt_pk_f16_f32 v223, v218, v219
	v_mfma_f32_32x32x16_f16 v[16:31], a[164:167], v[172:175], v[16:31]
	ds_read_b128 v[172:175], v193 offset:27648
	global_load_lds_dwordx4 v192, s[44:45] offset:1024 sc1
	s_nop 1
	v_permlane32_swap_b32_e32 v220, v222
	v_permlane32_swap_b32_e32 v221, v223
	s_cmp_eq_u32 s31, 0
	s_cbranch_scc1 .LE_slow22
	global_store_dwordx4 v195, v[220:223], s[36:37] offset:0
	s_branch .LE_join23

.LE_join25:
	v_mfma_f32_32x32x16_f16 v[16:31], a[192:195], v[164:167], v[16:31]
	ds_read_b128 v[164:167], v193 offset:41984
	v_mfma_f32_32x32x16_f16 v[0:15], a[196:199], v[168:171], v[0:15]
	ds_read_b128 v[168:171], v193 offset:43008
	v_mfma_f32_32x32x16_f16 v[16:31], a[196:199], v[172:175], v[16:31]
	ds_read_b128 v[172:175], v193 offset:44032
	global_load_lds_dwordx4 v192, s[44:45] offset:1024 sc1
	s_waitcnt lgkmcnt(4)
	v_mfma_f32_32x32x16_f16 v[0:15], a[200:203], v[176:179], v[0:15]
	ds_read_b128 v[176:179], v193 offset:45056
	v_mfma_f32_32x32x16_f16 v[16:31], a[200:203], v[180:183], v[16:31]
	ds_read_b128 v[180:183], v193 offset:46080
	v_mfma_f32_32x32x16_f16 v[0:15], a[204:207], v[184:187], v[0:15]
	ds_read_b128 v[184:187], v193 offset:47104
	v_mfma_f32_32x32x16_f16 v[16:31], a[204:207], v[188:191], v[16:31]
	ds_read_b128 v[188:191], v193 offset:48128
	global_load_lds_dwordx4 v192, s[44:45] offset:2048 sc1
	s_waitcnt lgkmcnt(4)
	v_mfma_f32_32x32x16_f16 v[0:15], a[208:211], v[160:163], v[0:15]
	ds_read_b128 v[160:163], v193 offset:49152
	v_mfma_f32_32x32x16_f16 v[16:31], a[208:211], v[164:167], v[16:31]
	ds_read_b128 v[164:167], v193 offset:50176
	v_mfma_f32_32x32x16_f16 v[0:15], a[212:215], v[168:171], v[0:15]
	ds_read_b128 v[168:171], v193 offset:51200
	v_mfma_f32_32x32x16_f16 v[16:31], a[212:215], v[172:175], v[16:31]
	ds_read_b128 v[172:175], v193 offset:52224
	global_load_lds_dwordx4 v192, s[44:45] offset:3072 sc1
	s_waitcnt lgkmcnt(4)
	v_mfma_f32_32x32x16_f16 v[0:15], a[216:219], v[176:179], v[0:15]
	ds_read_b128 v[176:179], v193 offset:53248
	v_mfma_f32_32x32x16_f16 v[16:31], a[216:219], v[180:183], v[16:31]
	ds_read_b128 v[180:183], v193 offset:54272
	v_mfma_f32_32x32x16_f16 v[0:15], a[220:223], v[184:187], v[0:15]
	ds_read_b128 v[184:187], v193 offset:55296
	v_mfma_f32_32x32x16_f16 v[16:31], a[220:223], v[188:191], v[16:31]
	ds_read_b128 v[188:191], v193 offset:56320
	s_add_u32 s44, s34, 0x9000
	s_addc_u32 s45, s35, 0
	s_mov_b32 m0, s55
	s_nop 0
	global_load_lds_dwordx4 v192, s[44:45] sc1
	s_waitcnt lgkmcnt(4)
	v_mfma_f32_32x32x16_f16 v[0:15], a[224:227], v[160:163], v[0:15]
	ds_read_b128 v[160:163], v193 offset:57344
	v_mfma_f32_32x32x16_f16 v[16:31], a[224:227], v[164:167], v[16:31]
	ds_read_b128 v[164:167], v193 offset:58368
	v_mfma_f32_32x32x16_f16 v[0:15], a[228:231], v[168:171], v[0:15]
	ds_read_b128 v[168:171], v193 offset:59392
	v_mfma_f32_32x32x16_f16 v[16:31], a[228:231], v[172:175], v[16:31]
	ds_read_b128 v[172:175], v193 offset:60416
	global_load_lds_dwordx4 v192, s[44:45] offset:1024 sc1
	s_waitcnt lgkmcnt(4)
	v_mfma_f32_32x32x16_f16 v[0:15], a[232:235], v[176:179], v[0:15]
	ds_read_b128 v[176:179], v193 offset:61440
	v_mfma_f32_32x32x16_f16 v[16:31], a[232:235], v[180:183], v[16:31]
	ds_read_b128 v[180:183], v193 offset:62464
	v_mfma_f32_32x32x16_f16 v[0:15], a[236:239], v[184:187], v[0:15]
	ds_read_b128 v[184:187], v193 offset:63488
	v_mfma_f32_32x32x16_f16 v[16:31], a[236:239], v[188:191], v[16:31]
	ds_read_b128 v[188:191], v193 offset:64512
	global_load_lds_dwordx4 v192, s[44:45] offset:2048 sc1
	s_waitcnt vmcnt(8)
	s_barrier
	s_waitcnt lgkmcnt(4)
	v_mfma_f32_32x32x16_f16 v[0:15], a[240:243], v[160:163], v[0:15]
	ds_read_b128 v[160:163], v192 offset:0
	v_mfma_f32_32x32x16_f16 v[16:31], a[240:243], v[164:167], v[16:31]
	ds_read_b128 v[164:167], v192 offset:1024
	v_mfma_f32_32x32x16_f16 v[0:15], a[244:247], v[168:171], v[0:15]
	ds_read_b128 v[168:171], v192 offset:2048
	v_mfma_f32_32x32x16_f16 v[16:31], a[244:247], v[172:175], v[16:31]
	ds_read_b128 v[172:175], v192 offset:3072
	global_load_lds_dwordx4 v192, s[44:45] offset:3072 sc1
	s_waitcnt lgkmcnt(4)
	v_mfma_f32_32x32x16_f16 v[0:15], a[248:251], v[176:179], v[0:15]
	ds_read_b128 v[176:179], v192 offset:4096
	v_mfma_f32_32x32x16_f16 v[16:31], a[248:251], v[180:183], v[16:31]
	ds_read_b128 v[180:183], v192 offset:5120
	v_mfma_f32_32x32x16_f16 v[0:15], a[252:255], v[184:187], v[0:15]
	ds_read_b128 v[184:187], v192 offset:6144
	v_mfma_f32_32x32x16_f16 v[16:31], a[252:255], v[188:191], v[16:31]
	ds_read_b128 v[188:191], v192 offset:7168
	s_add_u32 s44, s34, 0x10000
	s_addc_u32 s45, s35, 0
	s_mov_b32 m0, s56
	s_nop 0
	global_load_lds_dwordx4 v192, s[44:45] sc1
	s_and_b32 s64, s33, 1
	s_lshl_b32 s64, s64, 22
	s_add_u32 s64, s64, s50
	s_add_u32 s36, s6, s64
	s_addc_u32 s37, s7, 0
	s_lshl_b32 s64, s33, 3
	s_add_u32 s64, s64, s29
	s_lshl_b32 s64, s64, 5
	s_add_u32 s64, s64, s30
	s_lshl_b32 s64, s64, 2
	s_add_u32 s40, s8, s64
	s_addc_u32 s41, s9, 0
	s_lshl_b32 s64, s33, 11
	s_lshl_b32 s65, s29, 8
	s_add_u32 s64, s64, s65
	s_add_u32 s64, s64, 192
	s_lshl_b32 s64, s64, 3
	s_add_u32 s42, s12, s64
	s_addc_u32 s43, s13, 0
	s_nop 3
	global_load_dword v228, v249, s[42:43] offset:0
	global_load_dword v229, v249, s[42:43] offset:256
	s_waitcnt lgkmcnt(4)
	v_mfma_f32_32x32x16_f16 v[32:47], a[0:3], v[160:163], v[32:47]
	ds_read_b128 v[160:163], v192 offset:8192
	v_exp_f32_e32 v200, v0
	v_mfma_f32_32x32x16_f16 v[48:63], a[0:3], v[164:167], v[48:63]
	ds_read_b128 v[164:167], v192 offset:9216
	s_lshl_b32 s64, s71, 3
	s_add_u32 s64, s64, s29
	s_lshl_b32 s64, s64, 7
	s_add_u32 s38, s8, s64
	s_addc_u32 s39, s9, 0
	global_load_dword v251, v196, s[38:39] sc1
	v_exp_f32_e32 v201, v1
	v_add_f32_e32 v200, 1.0, v200
	v_mfma_f32_32x32x16_f16 v[32:47], a[4:7], v[168:171], v[32:47]
	ds_read_b128 v[168:171], v192 offset:10240
	v_exp_f32_e32 v202, v2
	v_add_f32_e32 v201, 1.0, v201
	v_mfma_f32_32x32x16_f16 v[48:63], a[4:7], v[172:175], v[48:63]
	ds_read_b128 v[172:175], v192 offset:11264
	global_load_lds_dwordx4 v192, s[44:45] offset:1024 sc1
	v_exp_f32_e32 v203, v3
	v_add_f32_e32 v202, 1.0, v202
	s_waitcnt lgkmcnt(4)
	v_mfma_f32_32x32x16_f16 v[32:47], a[8:11], v[176:179], v[32:47]
	ds_read_b128 v[176:179], v192 offset:12288
	v_exp_f32_e32 v204, v4
	v_add_f32_e32 v203, 1.0, v203
	v_mfma_f32_32x32x16_f16 v[48:63], a[8:11], v[180:183], v[48:63]
	ds_read_b128 v[180:183], v192 offset:13312
	v_exp_f32_e32 v205, v5
	v_add_f32_e32 v204, 1.0, v204
	v_mfma_f32_32x32x16_f16 v[32:47], a[12:15], v[184:187], v[32:47]
	ds_read_b128 v[184:187], v192 offset:14336
	v_exp_f32_e32 v206, v6
	v_add_f32_e32 v205, 1.0, v205
	v_mfma_f32_32x32x16_f16 v[48:63], a[12:15], v[188:191], v[48:63]
	ds_read_b128 v[188:191], v192 offset:15360
	global_load_lds_dwordx4 v192, s[44:45] offset:2048 sc1
	v_exp_f32_e32 v207, v7
	v_add_f32_e32 v206, 1.0, v206
	s_waitcnt lgkmcnt(4)
	v_mfma_f32_32x32x16_f16 v[32:47], a[16:19], v[160:163], v[32:47]
	ds_read_b128 v[160:163], v192 offset:16384
	v_exp_f32_e32 v208, v8
	v_add_f32_e32 v207, 1.0, v207
	v_mfma_f32_32x32x16_f16 v[48:63], a[16:19], v[164:167], v[48:63]
	ds_read_b128 v[164:167], v192 offset:17408
	v_exp_f32_e32 v209, v9
	v_add_f32_e32 v208, 1.0, v208
	v_mfma_f32_32x32x16_f16 v[32:47], a[20:23], v[168:171], v[32:47]
	ds_read_b128 v[168:171], v192 offset:18432
	v_exp_f32_e32 v210, v10
	v_add_f32_e32 v209, 1.0, v209
	v_mfma_f32_32x32x16_f16 v[48:63], a[20:23], v[172:175], v[48:63]
	ds_read_b128 v[172:175], v192 offset:19456
	global_load_lds_dwordx4 v192, s[44:45] offset:3072 sc1
	v_exp_f32_e32 v211, v11
	v_add_f32_e32 v210, 1.0, v210
	s_waitcnt lgkmcnt(4)
	v_mfma_f32_32x32x16_f16 v[32:47], a[24:27], v[176:179], v[32:47]
	ds_read_b128 v[176:179], v192 offset:20480
	v_exp_f32_e32 v212, v12
	v_add_f32_e32 v211, 1.0, v211
	v_mfma_f32_32x32x16_f16 v[48:63], a[24:27], v[180:183], v[48:63]
	ds_read_b128 v[180:183], v192 offset:21504
	v_exp_f32_e32 v213, v13
	v_add_f32_e32 v212, 1.0, v212
	v_mfma_f32_32x32x16_f16 v[32:47], a[28:31], v[184:187], v[32:47]
	ds_read_b128 v[184:187], v192 offset:22528
	v_exp_f32_e32 v214, v14
	v_add_f32_e32 v213, 1.0, v213
	v_mfma_f32_32x32x16_f16 v[48:63], a[28:31], v[188:191], v[48:63]
	ds_read_b128 v[188:191], v192 offset:23552
	s_add_u32 s44, s34, 0x11000
	s_addc_u32 s45, s35, 0
	s_mov_b32 m0, s57
	s_nop 0
	global_load_lds_dwordx4 v192, s[44:45] sc1
	v_exp_f32_e32 v215, v15
	v_add_f32_e32 v214, 1.0, v214
	s_waitcnt lgkmcnt(4)
	v_mfma_f32_32x32x16_f16 v[32:47], a[32:35], v[160:163], v[32:47]
	ds_read_b128 v[160:163], v192 offset:24576
	v_add_f32_e32 v215, 1.0, v215
	v_rcp_f32_e32 v200, v200
	v_mfma_f32_32x32x16_f16 v[48:63], a[32:35], v[164:167], v[48:63]
	ds_read_b128 v[164:167], v192 offset:25600
	v_rcp_f32_e32 v201, v201
	v_mfma_f32_32x32x16_f16 v[32:47], a[36:39], v[168:171], v[32:47]
	ds_read_b128 v[168:171], v192 offset:26624
	v_rcp_f32_e32 v202, v202
	v_mfma_f32_32x32x16_f16 v[48:63], a[36:39], v[172:175], v[48:63]
	ds_read_b128 v[172:175], v192 offset:27648
	global_load_lds_dwordx4 v192, s[44:45] offset:1024 sc1
	v_rcp_f32_e32 v203, v203
	s_waitcnt lgkmcnt(4)
	v_mfma_f32_32x32x16_f16 v[32:47], a[40:43], v[176:179], v[32:47]
	ds_read_b128 v[176:179], v192 offset:28672
	v_rcp_f32_e32 v204, v204
	v_mfma_f32_32x32x16_f16 v[48:63], a[40:43], v[180:183], v[48:63]
	ds_read_b128 v[180:183], v192 offset:29696
	v_rcp_f32_e32 v205, v205
	v_mul_f32_e32 v204, v204, v128
	v_mfma_f32_32x32x16_f16 v[32:47], a[44:47], v[184:187], v[32:47]
	ds_read_b128 v[184:187], v192 offset:30720
	v_rcp_f32_e32 v206, v206
	v_mul_f32_e32 v205, v205, v129
	v_mfma_f32_32x32x16_f16 v[48:63], a[44:47], v[188:191], v[48:63]
	ds_read_b128 v[188:191], v192 offset:31744
	global_load_lds_dwordx4 v192, s[44:45] offset:2048 sc1
	v_rcp_f32_e32 v207, v207
	v_mul_f32_e32 v206, v206, v130
	s_waitcnt vmcnt(10)
	s_barrier
	s_waitcnt lgkmcnt(4)
	v_mfma_f32_32x32x16_f16 v[32:47], a[48:51], v[160:163], v[32:47]
	ds_read_b128 v[160:163], v192 offset:32768
	v_rcp_f32_e32 v208, v208
	v_mul_f32_e32 v207, v207, v131
	v_mfma_f32_32x32x16_f16 v[48:63], a[48:51], v[164:167], v[48:63]
	ds_read_b128 v[164:167], v192 offset:33792
	v_rcp_f32_e32 v209, v209
	v_fmamk_f32 v208, v208, 0xc0b8aa3b, v198
	v_mfma_f32_32x32x16_f16 v[32:47], a[52:55], v[168:171], v[32:47]
	ds_read_b128 v[168:171], v192 offset:34816
	v_rcp_f32_e32 v210, v210
	v_fmamk_f32 v209, v209, 0xc0b8aa3b, v198
	v_fma_f32 v128, v200, v208, v204
	v_mfma_f32_32x32x16_f16 v[48:63], a[52:55], v[172:175], v[48:63]
	ds_read_b128 v[172:175], v192 offset:35840
	global_load_lds_dwordx4 v192, s[44:45] offset:3072 sc1
	v_rcp_f32_e32 v211, v211
	v_fmamk_f32 v210, v210, 0xc0b8aa3b, v198
	v_fma_f32 v129, v201, v209, v205
	s_waitcnt lgkmcnt(4)
	v_mfma_f32_32x32x16_f16 v[32:47], a[56:59], v[176:179], v[32:47]
	ds_read_b128 v[176:179], v192 offset:36864
	v_rcp_f32_e32 v212, v212
	v_fmamk_f32 v211, v211, 0xc0b8aa3b, v198
	v_fma_f32 v130, v202, v210, v206
	v_mfma_f32_32x32x16_f16 v[48:63], a[56:59], v[180:183], v[48:63]
	ds_read_b128 v[180:183], v192 offset:37888
	v_rcp_f32_e32 v213, v213
	v_fma_f32 v131, v203, v211, v207
	v_mfma_f32_32x32x16_f16 v[32:47], a[60:63], v[184:187], v[32:47]
	ds_read_b128 v[184:187], v192 offset:38912
	v_rcp_f32_e32 v214, v214
	v_mfma_f32_32x32x16_f16 v[48:63], a[60:63], v[188:191], v[48:63]
	ds_read_b128 v[188:191], v192 offset:39936
	s_add_u32 s44, s34, 0x18000
	s_addc_u32 s45, s35, 0
	s_mov_b32 m0, s58
	s_nop 0
	global_load_lds_dwordx4 v192, s[44:45] sc1
	v_rcp_f32_e32 v215, v215
	s_waitcnt lgkmcnt(4)
	v_mfma_f32_32x32x16_f16 v[32:47], a[64:67], v[160:163], v[32:47]
	ds_read_b128 v[160:163], v192 offset:40960
	v_exp_f32_e32 v200, v128
	v_mfma_f32_32x32x16_f16 v[48:63], a[64:67], v[164:167], v[48:63]
	ds_read_b128 v[164:167], v192 offset:41984
	v_exp_f32_e32 v201, v129
	v_add_f32_e32 v200, 1.0, v200
	v_mfma_f32_32x32x16_f16 v[32:47], a[68:71], v[168:171], v[32:47]
	ds_read_b128 v[168:171], v192 offset:43008
	v_exp_f32_e32 v202, v130
	v_add_f32_e32 v201, 1.0, v201
	v_mfma_f32_32x32x16_f16 v[48:63], a[68:71], v[172:175], v[48:63]
	ds_read_b128 v[172:175], v192 offset:44032
	global_load_lds_dwordx4 v192, s[44:45] offset:1024 sc1
	v_exp_f32_e32 v203, v131
	v_add_f32_e32 v202, 1.0, v202
	s_waitcnt lgkmcnt(4)
	v_mfma_f32_32x32x16_f16 v[32:47], a[72:75], v[176:179], v[32:47]
	ds_read_b128 v[176:179], v192 offset:45056
	v_add_f32_e32 v203, 1.0, v203
	v_rcp_f32_e32 v200, v200
	v_mfma_f32_32x32x16_f16 v[48:63], a[72:75], v[180:183], v[48:63]
	ds_read_b128 v[180:183], v192 offset:46080
	v_rcp_f32_e32 v201, v201
	v_fma_f32 v200, v200, 2.0, -1.0
	v_mfma_f32_32x32x16_f16 v[32:47], a[76:79], v[184:187], v[32:47]
	ds_read_b128 v[184:187], v192 offset:47104
	v_rcp_f32_e32 v202, v202
	v_fma_f32 v201, v201, 2.0, -1.0
	v_mul_f32_e32 v216, v212, v200
	v_mfma_f32_32x32x16_f16 v[48:63], a[76:79], v[188:191], v[48:63]
	ds_read_b128 v[188:191], v192 offset:48128
	global_load_lds_dwordx4 v192, s[44:45] offset:2048 sc1
	v_rcp_f32_e32 v203, v203
	v_fma_f32 v202, v202, 2.0, -1.0
	v_mul_f32_e32 v217, v213, v201
	s_waitcnt lgkmcnt(4)
	v_mfma_f32_32x32x16_f16 v[32:47], a[80:83], v[160:163], v[32:47]
	ds_read_b128 v[160:163], v192 offset:49152
	v_fma_f32 v203, v203, 2.0, -1.0
	v_mul_f32_e32 v218, v214, v202
	v_exp_f32_e32 v200, v16
	v_mfma_f32_32x32x16_f16 v[48:63], a[80:83], v[164:167], v[48:63]
	ds_read_b128 v[164:167], v192 offset:50176
	v_mul_f32_e32 v219, v215, v203
	v_cvt_pk_f16_f32 v220, v216, v217
	v_exp_f32_e32 v201, v17
	v_mfma_f32_32x32x16_f16 v[32:47], a[84:87], v[168:171], v[32:47]
	ds_read_b128 v[168:171], v192 offset:51200
	v_cvt_pk_f16_f32 v221, v218, v219
	v_exp_f32_e32 v202, v18
	v_add_f32_e32 v200, 1.0, v200
	v_mfma_f32_32x32x16_f16 v[48:63], a[84:87], v[172:175], v[48:63]
	ds_read_b128 v[172:175], v192 offset:52224
	global_load_lds_dwordx4 v192, s[44:45] offset:3072 sc1
	s_cmp_lg_u32 s33, s60
	s_cbranch_scc1 .LE_nht26
	s_add_u32 s46, s62, 0x0
	s_addc_u32 s47, s63, 0
	global_store_dwordx4 v250, v[216:219], s[46:47]
	s_waitcnt vmcnt(0)
.LE_nht26:
	v_exp_f32_e32 v203, v19
	s_waitcnt lgkmcnt(4)
	v_mfma_f32_32x32x16_f16 v[32:47], a[88:91], v[176:179], v[32:47]
	ds_read_b128 v[176:179], v192 offset:53248
	v_exp_f32_e32 v204, v20
	v_add_f32_e32 v201, 1.0, v201
	v_add_f32_e32 v202, 1.0, v202
	v_mfma_f32_32x32x16_f16 v[48:63], a[88:91], v[180:183], v[48:63]
	ds_read_b128 v[180:183], v192 offset:54272
	v_exp_f32_e32 v205, v21
	v_add_f32_e32 v203, 1.0, v203
	v_add_f32_e32 v204, 1.0, v204
	v_mfma_f32_32x32x16_f16 v[32:47], a[92:95], v[184:187], v[32:47]
	ds_read_b128 v[184:187], v192 offset:55296
	v_exp_f32_e32 v206, v22
	v_add_f32_e32 v205, 1.0, v205
	v_mfma_f32_32x32x16_f16 v[48:63], a[92:95], v[188:191], v[48:63]
	ds_read_b128 v[188:191], v192 offset:56320
	s_add_u32 s44, s34, 0x19000
	s_addc_u32 s45, s35, 0
	s_mov_b32 m0, s59
	s_nop 0
	global_load_lds_dwordx4 v192, s[44:45] sc1
	v_exp_f32_e32 v207, v23
	v_add_f32_e32 v206, 1.0, v206
	s_waitcnt lgkmcnt(4)
	v_mfma_f32_32x32x16_f16 v[32:47], a[96:99], v[160:163], v[32:47]
	ds_read_b128 v[160:163], v192 offset:57344
	v_exp_f32_e32 v208, v24
	v_add_f32_e32 v207, 1.0, v207
	v_mfma_f32_32x32x16_f16 v[48:63], a[96:99], v[164:167], v[48:63]
	ds_read_b128 v[164:167], v192 offset:58368
	v_exp_f32_e32 v209, v25
	v_add_f32_e32 v208, 1.0, v208
	v_mfma_f32_32x32x16_f16 v[32:47], a[100:103], v[168:171], v[32:47]
	ds_read_b128 v[168:171], v192 offset:59392
	v_exp_f32_e32 v210, v26
	v_add_f32_e32 v209, 1.0, v209
	v_mfma_f32_32x32x16_f16 v[48:63], a[100:103], v[172:175], v[48:63]
	ds_read_b128 v[172:175], v192 offset:60416
	global_load_lds_dwordx4 v192, s[44:45] offset:1024 sc1
	v_exp_f32_e32 v211, v27
	v_add_f32_e32 v210, 1.0, v210
	s_waitcnt lgkmcnt(4)
	v_mfma_f32_32x32x16_f16 v[32:47], a[104:107], v[176:179], v[32:47]
	ds_read_b128 v[176:179], v192 offset:61440
	v_exp_f32_e32 v212, v28
	v_add_f32_e32 v211, 1.0, v211
	v_mfma_f32_32x32x16_f16 v[48:63], a[104:107], v[180:183], v[48:63]
	ds_read_b128 v[180:183], v192 offset:62464
	v_exp_f32_e32 v213, v29
	v_add_f32_e32 v212, 1.0, v212
	v_mfma_f32_32x32x16_f16 v[32:47], a[108:111], v[184:187], v[32:47]
	ds_read_b128 v[184:187], v192 offset:63488
	v_exp_f32_e32 v214, v30
	v_add_f32_e32 v213, 1.0, v213
	v_mfma_f32_32x32x16_f16 v[48:63], a[108:111], v[188:191], v[48:63]
	ds_read_b128 v[188:191], v192 offset:64512
	global_load_lds_dwordx4 v192, s[44:45] offset:2048 sc1
	v_exp_f32_e32 v215, v31
	v_add_f32_e32 v214, 1.0, v214
	s_waitcnt vmcnt(7)
	s_barrier
	s_waitcnt lgkmcnt(4)
	v_mfma_f32_32x32x16_f16 v[32:47], a[112:115], v[160:163], v[32:47]
	ds_read_b128 v[160:163], v193 offset:0
	v_add_f32_e32 v215, 1.0, v215
	v_rcp_f32_e32 v200, v200
	v_mfma_f32_32x32x16_f16 v[48:63], a[112:115], v[164:167], v[48:63]
	ds_read_b128 v[164:167], v193 offset:1024
	v_rcp_f32_e32 v201, v201
	v_mfma_f32_32x32x16_f16 v[32:47], a[116:119], v[168:171], v[32:47]
	ds_read_b128 v[168:171], v193 offset:2048
	v_rcp_f32_e32 v202, v202
	v_mfma_f32_32x32x16_f16 v[48:63], a[116:119], v[172:175], v[48:63]
	ds_read_b128 v[172:175], v193 offset:3072
	global_load_lds_dwordx4 v192, s[44:45] offset:3072 sc1
	v_rcp_f32_e32 v203, v203
	s_waitcnt lgkmcnt(4)
	v_mfma_f32_32x32x16_f16 v[32:47], a[120:123], v[176:179], v[32:47]
	ds_read_b128 v[176:179], v193 offset:4096
	v_rcp_f32_e32 v204, v204
	v_mfma_f32_32x32x16_f16 v[48:63], a[120:123], v[180:183], v[48:63]
	ds_read_b128 v[180:183], v193 offset:5120
	v_rcp_f32_e32 v205, v205
	v_mul_f32_e32 v204, v204, v132
	v_mfma_f32_32x32x2_f32 v[96:111], v248, v228, v[232:247]
	v_mfma_f32_32x32x16_f16 v[32:47], a[124:127], v[184:187], v[32:47]
	ds_read_b128 v[184:187], v193 offset:6144
	v_rcp_f32_e32 v206, v206
	v_mul_f32_e32 v205, v205, v133
	v_mfma_f32_32x32x2_f32 v[112:127], v248, v229, v[232:247]
	v_mfma_f32_32x32x16_f16 v[48:63], a[124:127], v[188:191], v[48:63]
	ds_read_b128 v[188:191], v193 offset:7168
	v_cmp_gt_u32_e32 vcc, 3, v251
	s_cbranch_vccz .LE_tok27

.LE_tok27:
	s_and_b32 s64, s71, 1
	s_lshl_b32 s64, s64, 22
	s_add_u32 s64, s64, s49
	s_add_u32 s64, s64, 0x40000
	s_add_u32 s34, s6, s64
	s_addc_u32 s35, s7, 0
	s_add_u32 s44, s34, 0x0
	s_addc_u32 s45, s35, 0
	s_mov_b32 m0, s52
	s_nop 0
	global_load_lds_dwordx4 v192, s[44:45] sc1
	v_rcp_f32_e32 v207, v207
	v_mul_f32_e32 v206, v206, v134
	s_waitcnt lgkmcnt(4)
	v_mfma_f32_32x32x16_f16 v[32:47], a[128:131], v[160:163], v[32:47]
	ds_read_b128 v[160:163], v193 offset:8192
	v_rcp_f32_e32 v208, v208
	v_mul_f32_e32 v207, v207, v135
	v_mfma_f32_32x32x16_f16 v[48:63], a[128:131], v[164:167], v[48:63]
	ds_read_b128 v[164:167], v193 offset:9216
	v_rcp_f32_e32 v209, v209
	v_fmamk_f32 v208, v208, 0xc0b8aa3b, v198
	v_mfma_f32_32x32x16_f16 v[32:47], a[132:135], v[168:171], v[32:47]
	ds_read_b128 v[168:171], v193 offset:10240
	v_rcp_f32_e32 v210, v210
	v_fmamk_f32 v209, v209, 0xc0b8aa3b, v198
	v_fma_f32 v132, v200, v208, v204
	v_mfma_f32_32x32x16_f16 v[48:63], a[132:135], v[172:175], v[48:63]
	ds_read_b128 v[172:175], v193 offset:11264
	global_load_lds_dwordx4 v192, s[44:45] offset:1024 sc1
	v_rcp_f32_e32 v211, v211
	v_fmamk_f32 v210, v210, 0xc0b8aa3b, v198
	v_fma_f32 v133, v201, v209, v205
	s_waitcnt lgkmcnt(4)
	v_mfma_f32_32x32x16_f16 v[32:47], a[136:139], v[176:179], v[32:47]
	ds_read_b128 v[176:179], v193 offset:12288
	v_rcp_f32_e32 v212, v212
	v_fmamk_f32 v211, v211, 0xc0b8aa3b, v198
	v_fma_f32 v134, v202, v210, v206
	v_mfma_f32_32x32x16_f16 v[48:63], a[136:139], v[180:183], v[48:63]
	ds_read_b128 v[180:183], v193 offset:13312
	v_rcp_f32_e32 v213, v213
	v_fma_f32 v135, v203, v211, v207
	v_mfma_f32_32x32x16_f16 v[32:47], a[140:143], v[184:187], v[32:47]
	ds_read_b128 v[184:187], v193 offset:14336
	v_rcp_f32_e32 v214, v214
	v_mfma_f32_32x32x16_f16 v[48:63], a[140:143], v[188:191], v[48:63]
	ds_read_b128 v[188:191], v193 offset:15360
	global_load_lds_dwordx4 v192, s[44:45] offset:2048 sc1
	v_rcp_f32_e32 v215, v215
	s_waitcnt lgkmcnt(4)
	v_mfma_f32_32x32x16_f16 v[32:47], a[144:147], v[160:163], v[32:47]
	ds_read_b128 v[160:163], v193 offset:16384
	v_exp_f32_e32 v200, v132
	v_mfma_f32_32x32x16_f16 v[48:63], a[144:147], v[164:167], v[48:63]
	ds_read_b128 v[164:167], v193 offset:17408
	v_exp_f32_e32 v201, v133
	v_add_f32_e32 v200, 1.0, v200
	v_mfma_f32_32x32x16_f16 v[32:47], a[148:151], v[168:171], v[32:47]
	ds_read_b128 v[168:171], v193 offset:18432
	v_exp_f32_e32 v202, v134
	v_add_f32_e32 v201, 1.0, v201
	v_mfma_f32_32x32x16_f16 v[48:63], a[148:151], v[172:175], v[48:63]
	ds_read_b128 v[172:175], v193 offset:19456
	global_load_lds_dwordx4 v192, s[44:45] offset:3072 sc1
	v_exp_f32_e32 v203, v135
	v_add_f32_e32 v202, 1.0, v202
	s_waitcnt lgkmcnt(4)
	v_mfma_f32_32x32x16_f16 v[32:47], a[152:155], v[176:179], v[32:47]
	ds_read_b128 v[176:179], v193 offset:20480
	v_add_f32_e32 v203, 1.0, v203
	v_rcp_f32_e32 v200, v200
	v_mfma_f32_32x32x16_f16 v[48:63], a[152:155], v[180:183], v[48:63]
	ds_read_b128 v[180:183], v193 offset:21504
	v_rcp_f32_e32 v201, v201
	v_fma_f32 v200, v200, 2.0, -1.0
	v_mfma_f32_32x32x16_f16 v[32:47], a[156:159], v[184:187], v[32:47]
	ds_read_b128 v[184:187], v193 offset:22528
	v_rcp_f32_e32 v202, v202
	v_fma_f32 v201, v201, 2.0, -1.0
	v_mul_f32_e32 v216, v212, v200
	v_mfma_f32_32x32x16_f16 v[48:63], a[156:159], v[188:191], v[48:63]
	ds_read_b128 v[188:191], v193 offset:23552
	s_add_u32 s44, s34, 0x1000
	s_addc_u32 s45, s35, 0
	s_mov_b32 m0, s53
	s_nop 0
	global_load_lds_dwordx4 v192, s[44:45] sc1
	v_rcp_f32_e32 v203, v203
	v_fma_f32 v202, v202, 2.0, -1.0
	v_mul_f32_e32 v217, v213, v201
	s_waitcnt lgkmcnt(4)
	v_mfma_f32_32x32x16_f16 v[32:47], a[160:163], v[160:163], v[32:47]
	ds_read_b128 v[160:163], v193 offset:24576
	v_fma_f32 v203, v203, 2.0, -1.0
	v_mul_f32_e32 v218, v214, v202
	v_mfma_f32_32x32x16_f16 v[48:63], a[160:163], v[164:167], v[48:63]
	ds_read_b128 v[164:167], v193 offset:25600
	v_mul_f32_e32 v219, v215, v203
	v_cvt_pk_f16_f32 v222, v216, v217
	v_mfma_f32_32x32x16_f16 v[32:47], a[164:167], v[168:171], v[32:47]
	ds_read_b128 v[168:171], v193 offset:26624
	v_cvt_pk_f16_f32 v223, v218, v219
	v_mfma_f32_32x32x16_f16 v[48:63], a[164:167], v[172:175], v[48:63]
	ds_read_b128 v[172:175], v193 offset:27648
	global_load_lds_dwordx4 v192, s[44:45] offset:1024 sc1
	s_cmp_lg_u32 s33, s60
	s_cbranch_scc1 .LE_nht29
	s_add_u32 s46, s62, 0x20000
	s_addc_u32 s47, s63, 0
	global_store_dwordx4 v250, v[216:219], s[46:47]
	s_waitcnt vmcnt(0)

.LE_join33:
	v_mfma_f32_32x32x16_f16 v[32:47], a[196:199], v[168:171], v[32:47]
	ds_read_b128 v[168:171], v193 offset:43008
	v_mfma_f32_32x32x16_f16 v[48:63], a[196:199], v[172:175], v[48:63]
	ds_read_b128 v[172:175], v193 offset:44032
	global_load_lds_dwordx4 v192, s[44:45] offset:1024 sc1
	s_waitcnt lgkmcnt(4)
	v_mfma_f32_32x32x16_f16 v[32:47], a[200:203], v[176:179], v[32:47]
	ds_read_b128 v[176:179], v193 offset:45056
	v_mfma_f32_32x32x16_f16 v[48:63], a[200:203], v[180:183], v[48:63]
	ds_read_b128 v[180:183], v193 offset:46080
	v_mfma_f32_32x32x16_f16 v[32:47], a[204:207], v[184:187], v[32:47]
	ds_read_b128 v[184:187], v193 offset:47104
	v_mfma_f32_32x32x16_f16 v[48:63], a[204:207], v[188:191], v[48:63]
	ds_read_b128 v[188:191], v193 offset:48128
	global_load_lds_dwordx4 v192, s[44:45] offset:2048 sc1
	s_waitcnt lgkmcnt(4)
	v_mfma_f32_32x32x16_f16 v[32:47], a[208:211], v[160:163], v[32:47]
	ds_read_b128 v[160:163], v193 offset:49152
	v_mfma_f32_32x32x16_f16 v[48:63], a[208:211], v[164:167], v[48:63]
	ds_read_b128 v[164:167], v193 offset:50176
	v_mfma_f32_32x32x16_f16 v[32:47], a[212:215], v[168:171], v[32:47]
	ds_read_b128 v[168:171], v193 offset:51200
	v_mfma_f32_32x32x16_f16 v[48:63], a[212:215], v[172:175], v[48:63]
	ds_read_b128 v[172:175], v193 offset:52224
	global_load_lds_dwordx4 v192, s[44:45] offset:3072 sc1
	s_waitcnt lgkmcnt(4)
	v_mfma_f32_32x32x16_f16 v[32:47], a[216:219], v[176:179], v[32:47]
	ds_read_b128 v[176:179], v193 offset:53248
	v_mfma_f32_32x32x16_f16 v[48:63], a[216:219], v[180:183], v[48:63]
	ds_read_b128 v[180:183], v193 offset:54272
	v_mfma_f32_32x32x16_f16 v[32:47], a[220:223], v[184:187], v[32:47]
	ds_read_b128 v[184:187], v193 offset:55296
	v_mfma_f32_32x32x16_f16 v[48:63], a[220:223], v[188:191], v[48:63]
	ds_read_b128 v[188:191], v193 offset:56320
	s_add_u32 s44, s34, 0x9000
	s_addc_u32 s45, s35, 0
	s_mov_b32 m0, s55
	s_nop 0
	global_load_lds_dwordx4 v192, s[44:45] sc1
	s_waitcnt lgkmcnt(4)
	v_mfma_f32_32x32x16_f16 v[32:47], a[224:227], v[160:163], v[32:47]
	ds_read_b128 v[160:163], v193 offset:57344
	v_mfma_f32_32x32x16_f16 v[48:63], a[224:227], v[164:167], v[48:63]
	ds_read_b128 v[164:167], v193 offset:58368
	v_mfma_f32_32x32x16_f16 v[32:47], a[228:231], v[168:171], v[32:47]
	ds_read_b128 v[168:171], v193 offset:59392
	v_mfma_f32_32x32x16_f16 v[48:63], a[228:231], v[172:175], v[48:63]
	ds_read_b128 v[172:175], v193 offset:60416
	global_load_lds_dwordx4 v192, s[44:45] offset:1024 sc1
	s_waitcnt lgkmcnt(4)
	v_mfma_f32_32x32x16_f16 v[32:47], a[232:235], v[176:179], v[32:47]
	ds_read_b128 v[176:179], v193 offset:61440
	v_mfma_f32_32x32x16_f16 v[48:63], a[232:235], v[180:183], v[48:63]
	ds_read_b128 v[180:183], v193 offset:62464
	v_mfma_f32_32x32x16_f16 v[32:47], a[236:239], v[184:187], v[32:47]
	ds_read_b128 v[184:187], v193 offset:63488
	v_mfma_f32_32x32x16_f16 v[48:63], a[236:239], v[188:191], v[48:63]
	ds_read_b128 v[188:191], v193 offset:64512
	global_load_lds_dwordx4 v192, s[44:45] offset:2048 sc1
	s_waitcnt vmcnt(8)
	s_barrier
	s_waitcnt lgkmcnt(4)
	v_mfma_f32_32x32x16_f16 v[32:47], a[240:243], v[160:163], v[32:47]
	ds_read_b128 v[160:163], v192 offset:0
	v_mfma_f32_32x32x16_f16 v[48:63], a[240:243], v[164:167], v[48:63]
	ds_read_b128 v[164:167], v192 offset:1024
	v_mfma_f32_32x32x16_f16 v[32:47], a[244:247], v[168:171], v[32:47]
	ds_read_b128 v[168:171], v192 offset:2048
	v_mfma_f32_32x32x16_f16 v[48:63], a[244:247], v[172:175], v[48:63]
	ds_read_b128 v[172:175], v192 offset:3072
	global_load_lds_dwordx4 v192, s[44:45] offset:3072 sc1
	s_waitcnt lgkmcnt(4)
	v_mfma_f32_32x32x16_f16 v[32:47], a[248:251], v[176:179], v[32:47]
	ds_read_b128 v[176:179], v192 offset:4096
	v_mfma_f32_32x32x16_f16 v[48:63], a[248:251], v[180:183], v[48:63]
	ds_read_b128 v[180:183], v192 offset:5120
	v_mfma_f32_32x32x16_f16 v[32:47], a[252:255], v[184:187], v[32:47]
	ds_read_b128 v[184:187], v192 offset:6144
	v_mfma_f32_32x32x16_f16 v[48:63], a[252:255], v[188:191], v[48:63]
	ds_read_b128 v[188:191], v192 offset:7168
	s_add_u32 s44, s34, 0x10000
	s_addc_u32 s45, s35, 0
	s_mov_b32 m0, s56
	s_nop 0
	global_load_lds_dwordx4 v192, s[44:45] sc1
	s_and_b32 s64, s33, 1
	s_lshl_b32 s64, s64, 22
	s_add_u32 s64, s64, s50
	s_add_u32 s64, s64, 0x20000
	s_add_u32 s36, s6, s64
	s_addc_u32 s37, s7, 0
	s_lshl_b32 s64, s33, 3
	s_add_u32 s64, s64, s29
	s_lshl_b32 s64, s64, 5
	s_add_u32 s64, s64, s30
	s_lshl_b32 s64, s64, 2
	s_add_u32 s40, s8, s64
	s_addc_u32 s41, s9, 0
	s_lshl_b32 s64, s61, 11
	s_lshl_b32 s65, s29, 8
	s_add_u32 s64, s64, s65
	s_lshl_b32 s64, s64, 3
	s_add_u32 s42, s12, s64
	s_addc_u32 s43, s13, 0
	s_nop 3
	global_load_dword v228, v249, s[42:43] offset:0
	global_load_dword v229, v249, s[42:43] offset:256
	s_waitcnt lgkmcnt(4)
	v_mfma_f32_32x32x16_f16 v[64:79], a[0:3], v[160:163], v[64:79]
	ds_read_b128 v[160:163], v192 offset:8192
	v_exp_f32_e32 v200, v32
	v_mfma_f32_32x32x16_f16 v[80:95], a[0:3], v[164:167], v[80:95]
	ds_read_b128 v[164:167], v192 offset:9216
	s_lshl_b32 s64, s71, 3
	s_add_u32 s64, s64, s29
	s_lshl_b32 s64, s64, 7
	s_add_u32 s38, s8, s64
	s_addc_u32 s39, s9, 0
	global_load_dword v251, v196, s[38:39] sc1
	v_exp_f32_e32 v201, v33
	v_add_f32_e32 v200, 1.0, v200
	v_mfma_f32_32x32x16_f16 v[64:79], a[4:7], v[168:171], v[64:79]
	ds_read_b128 v[168:171], v192 offset:10240
	v_exp_f32_e32 v202, v34
	v_add_f32_e32 v201, 1.0, v201
	v_mfma_f32_32x32x16_f16 v[80:95], a[4:7], v[172:175], v[80:95]
	ds_read_b128 v[172:175], v192 offset:11264
	global_load_lds_dwordx4 v192, s[44:45] offset:1024 sc1
	v_exp_f32_e32 v203, v35
	v_add_f32_e32 v202, 1.0, v202
	s_waitcnt lgkmcnt(4)
	v_mfma_f32_32x32x16_f16 v[64:79], a[8:11], v[176:179], v[64:79]
	ds_read_b128 v[176:179], v192 offset:12288
	v_exp_f32_e32 v204, v36
	v_add_f32_e32 v203, 1.0, v203
	v_mfma_f32_32x32x16_f16 v[80:95], a[8:11], v[180:183], v[80:95]
	ds_read_b128 v[180:183], v192 offset:13312
	v_exp_f32_e32 v205, v37
	v_add_f32_e32 v204, 1.0, v204
	v_mfma_f32_32x32x16_f16 v[64:79], a[12:15], v[184:187], v[64:79]
	ds_read_b128 v[184:187], v192 offset:14336
	v_exp_f32_e32 v206, v38
	v_add_f32_e32 v205, 1.0, v205
	v_mfma_f32_32x32x16_f16 v[80:95], a[12:15], v[188:191], v[80:95]
	ds_read_b128 v[188:191], v192 offset:15360
	global_load_lds_dwordx4 v192, s[44:45] offset:2048 sc1
	v_exp_f32_e32 v207, v39
	v_add_f32_e32 v206, 1.0, v206
	s_waitcnt lgkmcnt(4)
	v_mfma_f32_32x32x16_f16 v[64:79], a[16:19], v[160:163], v[64:79]
	ds_read_b128 v[160:163], v192 offset:16384
	v_exp_f32_e32 v208, v40
	v_add_f32_e32 v207, 1.0, v207
	v_mfma_f32_32x32x16_f16 v[80:95], a[16:19], v[164:167], v[80:95]
	ds_read_b128 v[164:167], v192 offset:17408
	v_exp_f32_e32 v209, v41
	v_add_f32_e32 v208, 1.0, v208
	v_mfma_f32_32x32x16_f16 v[64:79], a[20:23], v[168:171], v[64:79]
	ds_read_b128 v[168:171], v192 offset:18432
	v_exp_f32_e32 v210, v42
	v_add_f32_e32 v209, 1.0, v209
	v_mfma_f32_32x32x16_f16 v[80:95], a[20:23], v[172:175], v[80:95]
	ds_read_b128 v[172:175], v192 offset:19456
	global_load_lds_dwordx4 v192, s[44:45] offset:3072 sc1
	v_exp_f32_e32 v211, v43
	v_add_f32_e32 v210, 1.0, v210
	s_waitcnt lgkmcnt(4)
	v_mfma_f32_32x32x16_f16 v[64:79], a[24:27], v[176:179], v[64:79]
	ds_read_b128 v[176:179], v192 offset:20480
	v_exp_f32_e32 v212, v44
	v_add_f32_e32 v211, 1.0, v211
	v_mfma_f32_32x32x16_f16 v[80:95], a[24:27], v[180:183], v[80:95]
	ds_read_b128 v[180:183], v192 offset:21504
	v_exp_f32_e32 v213, v45
	v_add_f32_e32 v212, 1.0, v212
	v_mfma_f32_32x32x16_f16 v[64:79], a[28:31], v[184:187], v[64:79]
	ds_read_b128 v[184:187], v192 offset:22528
	v_exp_f32_e32 v214, v46
	v_add_f32_e32 v213, 1.0, v213
	v_mfma_f32_32x32x16_f16 v[80:95], a[28:31], v[188:191], v[80:95]
	ds_read_b128 v[188:191], v192 offset:23552
	s_add_u32 s44, s34, 0x11000
	s_addc_u32 s45, s35, 0
	s_mov_b32 m0, s57
	s_nop 0
	global_load_lds_dwordx4 v192, s[44:45] sc1
	v_exp_f32_e32 v215, v47
	v_add_f32_e32 v214, 1.0, v214
	s_waitcnt lgkmcnt(4)
	v_mfma_f32_32x32x16_f16 v[64:79], a[32:35], v[160:163], v[64:79]
	ds_read_b128 v[160:163], v192 offset:24576
	v_add_f32_e32 v215, 1.0, v215
	v_rcp_f32_e32 v200, v200
	v_mfma_f32_32x32x16_f16 v[80:95], a[32:35], v[164:167], v[80:95]
	ds_read_b128 v[164:167], v192 offset:25600
	v_rcp_f32_e32 v201, v201
	v_mfma_f32_32x32x16_f16 v[64:79], a[36:39], v[168:171], v[64:79]
	ds_read_b128 v[168:171], v192 offset:26624
	v_rcp_f32_e32 v202, v202
	v_mfma_f32_32x32x16_f16 v[80:95], a[36:39], v[172:175], v[80:95]
	ds_read_b128 v[172:175], v192 offset:27648
	global_load_lds_dwordx4 v192, s[44:45] offset:1024 sc1
	v_rcp_f32_e32 v203, v203
	s_waitcnt lgkmcnt(4)
	v_mfma_f32_32x32x16_f16 v[64:79], a[40:43], v[176:179], v[64:79]
	ds_read_b128 v[176:179], v192 offset:28672
	v_rcp_f32_e32 v204, v204
	v_mfma_f32_32x32x16_f16 v[80:95], a[40:43], v[180:183], v[80:95]
	ds_read_b128 v[180:183], v192 offset:29696
	v_rcp_f32_e32 v205, v205
	v_mul_f32_e32 v204, v204, v136
	v_mfma_f32_32x32x16_f16 v[64:79], a[44:47], v[184:187], v[64:79]
	ds_read_b128 v[184:187], v192 offset:30720
	v_rcp_f32_e32 v206, v206
	v_mul_f32_e32 v205, v205, v137
	v_mfma_f32_32x32x16_f16 v[80:95], a[44:47], v[188:191], v[80:95]
	ds_read_b128 v[188:191], v192 offset:31744
	global_load_lds_dwordx4 v192, s[44:45] offset:2048 sc1
	v_rcp_f32_e32 v207, v207
	v_mul_f32_e32 v206, v206, v138
	s_waitcnt vmcnt(10)
	s_barrier
	s_waitcnt lgkmcnt(4)
	v_mfma_f32_32x32x16_f16 v[64:79], a[48:51], v[160:163], v[64:79]
	ds_read_b128 v[160:163], v192 offset:32768
	v_rcp_f32_e32 v208, v208
	v_mul_f32_e32 v207, v207, v139
	v_mfma_f32_32x32x16_f16 v[80:95], a[48:51], v[164:167], v[80:95]
	ds_read_b128 v[164:167], v192 offset:33792
	v_rcp_f32_e32 v209, v209
	v_fmamk_f32 v208, v208, 0xc0b8aa3b, v198
	v_mfma_f32_32x32x16_f16 v[64:79], a[52:55], v[168:171], v[64:79]
	ds_read_b128 v[168:171], v192 offset:34816
	v_rcp_f32_e32 v210, v210
	v_fmamk_f32 v209, v209, 0xc0b8aa3b, v198
	v_fma_f32 v136, v200, v208, v204
	v_mfma_f32_32x32x16_f16 v[80:95], a[52:55], v[172:175], v[80:95]
	ds_read_b128 v[172:175], v192 offset:35840
	global_load_lds_dwordx4 v192, s[44:45] offset:3072 sc1
	v_rcp_f32_e32 v211, v211
	v_fmamk_f32 v210, v210, 0xc0b8aa3b, v198
	v_fma_f32 v137, v201, v209, v205
	s_waitcnt lgkmcnt(4)
	v_mfma_f32_32x32x16_f16 v[64:79], a[56:59], v[176:179], v[64:79]
	ds_read_b128 v[176:179], v192 offset:36864
	v_rcp_f32_e32 v212, v212
	v_fmamk_f32 v211, v211, 0xc0b8aa3b, v198
	v_fma_f32 v138, v202, v210, v206
	v_mfma_f32_32x32x16_f16 v[80:95], a[56:59], v[180:183], v[80:95]
	ds_read_b128 v[180:183], v192 offset:37888
	v_rcp_f32_e32 v213, v213
	v_fma_f32 v139, v203, v211, v207
	v_mfma_f32_32x32x16_f16 v[64:79], a[60:63], v[184:187], v[64:79]
	ds_read_b128 v[184:187], v192 offset:38912
	v_rcp_f32_e32 v214, v214
	v_mfma_f32_32x32x16_f16 v[80:95], a[60:63], v[188:191], v[80:95]
	ds_read_b128 v[188:191], v192 offset:39936
	s_add_u32 s44, s34, 0x18000
	s_addc_u32 s45, s35, 0
	s_mov_b32 m0, s58
	s_nop 0
	global_load_lds_dwordx4 v192, s[44:45] sc1
	v_rcp_f32_e32 v215, v215
	s_waitcnt lgkmcnt(4)
	v_mfma_f32_32x32x16_f16 v[64:79], a[64:67], v[160:163], v[64:79]
	ds_read_b128 v[160:163], v192 offset:40960
	v_exp_f32_e32 v200, v136
	v_mfma_f32_32x32x16_f16 v[80:95], a[64:67], v[164:167], v[80:95]
	ds_read_b128 v[164:167], v192 offset:41984
	v_exp_f32_e32 v201, v137
	v_add_f32_e32 v200, 1.0, v200
	v_mfma_f32_32x32x16_f16 v[64:79], a[68:71], v[168:171], v[64:79]
	ds_read_b128 v[168:171], v192 offset:43008
	v_exp_f32_e32 v202, v138
	v_add_f32_e32 v201, 1.0, v201
	v_mfma_f32_32x32x16_f16 v[80:95], a[68:71], v[172:175], v[80:95]
	ds_read_b128 v[172:175], v192 offset:44032
	global_load_lds_dwordx4 v192, s[44:45] offset:1024 sc1
	v_exp_f32_e32 v203, v139
	v_add_f32_e32 v202, 1.0, v202
	s_waitcnt lgkmcnt(4)
	v_mfma_f32_32x32x16_f16 v[64:79], a[72:75], v[176:179], v[64:79]
	ds_read_b128 v[176:179], v192 offset:45056
	v_add_f32_e32 v203, 1.0, v203
	v_rcp_f32_e32 v200, v200
	v_mfma_f32_32x32x16_f16 v[80:95], a[72:75], v[180:183], v[80:95]
	ds_read_b128 v[180:183], v192 offset:46080
	v_rcp_f32_e32 v201, v201
	v_fma_f32 v200, v200, 2.0, -1.0
	v_mfma_f32_32x32x16_f16 v[64:79], a[76:79], v[184:187], v[64:79]
	ds_read_b128 v[184:187], v192 offset:47104
	v_rcp_f32_e32 v202, v202
	v_fma_f32 v201, v201, 2.0, -1.0
	v_mul_f32_e32 v216, v212, v200
	v_mfma_f32_32x32x16_f16 v[80:95], a[76:79], v[188:191], v[80:95]
	ds_read_b128 v[188:191], v192 offset:48128
	global_load_lds_dwordx4 v192, s[44:45] offset:2048 sc1
	v_rcp_f32_e32 v203, v203
	v_fma_f32 v202, v202, 2.0, -1.0
	v_mul_f32_e32 v217, v213, v201
	s_waitcnt lgkmcnt(4)
	v_mfma_f32_32x32x16_f16 v[64:79], a[80:83], v[160:163], v[64:79]
	ds_read_b128 v[160:163], v192 offset:49152
	v_fma_f32 v203, v203, 2.0, -1.0
	v_mul_f32_e32 v218, v214, v202
	v_exp_f32_e32 v200, v48
	v_mfma_f32_32x32x16_f16 v[80:95], a[80:83], v[164:167], v[80:95]
	ds_read_b128 v[164:167], v192 offset:50176
	v_mul_f32_e32 v219, v215, v203
	v_cvt_pk_f16_f32 v220, v216, v217
	v_exp_f32_e32 v201, v49
	v_mfma_f32_32x32x16_f16 v[64:79], a[84:87], v[168:171], v[64:79]
	ds_read_b128 v[168:171], v192 offset:51200
	v_cvt_pk_f16_f32 v221, v218, v219
	v_exp_f32_e32 v202, v50
	v_add_f32_e32 v200, 1.0, v200
	v_mfma_f32_32x32x16_f16 v[80:95], a[84:87], v[172:175], v[80:95]
	ds_read_b128 v[172:175], v192 offset:52224
	global_load_lds_dwordx4 v192, s[44:45] offset:3072 sc1
	s_cmp_lg_u32 s33, s60
	s_cbranch_scc1 .LE_nht34
	s_add_u32 s46, s62, 0x40000
	s_addc_u32 s47, s63, 0
	global_store_dwordx4 v250, v[216:219], s[46:47]
	s_waitcnt vmcnt(0)
.LE_nht34:
	v_exp_f32_e32 v203, v51
	s_waitcnt lgkmcnt(4)
	v_mfma_f32_32x32x16_f16 v[64:79], a[88:91], v[176:179], v[64:79]
	ds_read_b128 v[176:179], v192 offset:53248
	v_exp_f32_e32 v204, v52
	v_add_f32_e32 v201, 1.0, v201
	v_add_f32_e32 v202, 1.0, v202
	v_mfma_f32_32x32x16_f16 v[80:95], a[88:91], v[180:183], v[80:95]
	ds_read_b128 v[180:183], v192 offset:54272
	v_exp_f32_e32 v205, v53
	v_add_f32_e32 v203, 1.0, v203
	v_add_f32_e32 v204, 1.0, v204
	v_mfma_f32_32x32x16_f16 v[64:79], a[92:95], v[184:187], v[64:79]
	ds_read_b128 v[184:187], v192 offset:55296
	v_exp_f32_e32 v206, v54
	v_add_f32_e32 v205, 1.0, v205
	v_mfma_f32_32x32x16_f16 v[80:95], a[92:95], v[188:191], v[80:95]
	ds_read_b128 v[188:191], v192 offset:56320
	s_add_u32 s44, s34, 0x19000
	s_addc_u32 s45, s35, 0
	s_mov_b32 m0, s59
	s_nop 0
	global_load_lds_dwordx4 v192, s[44:45] sc1
	v_exp_f32_e32 v207, v55
	v_add_f32_e32 v206, 1.0, v206
	s_waitcnt lgkmcnt(4)
	v_mfma_f32_32x32x16_f16 v[64:79], a[96:99], v[160:163], v[64:79]
	ds_read_b128 v[160:163], v192 offset:57344
	v_exp_f32_e32 v208, v56
	v_add_f32_e32 v207, 1.0, v207
	v_mfma_f32_32x32x16_f16 v[80:95], a[96:99], v[164:167], v[80:95]
	ds_read_b128 v[164:167], v192 offset:58368
	v_exp_f32_e32 v209, v57
	v_add_f32_e32 v208, 1.0, v208
	v_mfma_f32_32x32x16_f16 v[64:79], a[100:103], v[168:171], v[64:79]
	ds_read_b128 v[168:171], v192 offset:59392
	v_exp_f32_e32 v210, v58
	v_add_f32_e32 v209, 1.0, v209
	v_mfma_f32_32x32x16_f16 v[80:95], a[100:103], v[172:175], v[80:95]
	ds_read_b128 v[172:175], v192 offset:60416
	global_load_lds_dwordx4 v192, s[44:45] offset:1024 sc1
	v_exp_f32_e32 v211, v59
	v_add_f32_e32 v210, 1.0, v210
	s_waitcnt lgkmcnt(4)
	v_mfma_f32_32x32x16_f16 v[64:79], a[104:107], v[176:179], v[64:79]
	ds_read_b128 v[176:179], v192 offset:61440
	v_exp_f32_e32 v212, v60
	v_add_f32_e32 v211, 1.0, v211
	v_mfma_f32_32x32x16_f16 v[80:95], a[104:107], v[180:183], v[80:95]
	ds_read_b128 v[180:183], v192 offset:62464
	v_exp_f32_e32 v213, v61
	v_add_f32_e32 v212, 1.0, v212
	v_mfma_f32_32x32x16_f16 v[64:79], a[108:111], v[184:187], v[64:79]
	ds_read_b128 v[184:187], v192 offset:63488
	v_exp_f32_e32 v214, v62
	v_add_f32_e32 v213, 1.0, v213
	v_mfma_f32_32x32x16_f16 v[80:95], a[108:111], v[188:191], v[80:95]
	ds_read_b128 v[188:191], v192 offset:64512
	global_load_lds_dwordx4 v192, s[44:45] offset:2048 sc1
	v_exp_f32_e32 v215, v63
	v_add_f32_e32 v214, 1.0, v214
	s_waitcnt vmcnt(7)
	s_barrier
	s_waitcnt lgkmcnt(4)
	v_mfma_f32_32x32x16_f16 v[64:79], a[112:115], v[160:163], v[64:79]
	ds_read_b128 v[160:163], v193 offset:0
	v_add_f32_e32 v215, 1.0, v215
	v_rcp_f32_e32 v200, v200
	v_mfma_f32_32x32x16_f16 v[80:95], a[112:115], v[164:167], v[80:95]
	ds_read_b128 v[164:167], v193 offset:1024
	v_rcp_f32_e32 v201, v201
	v_mfma_f32_32x32x16_f16 v[64:79], a[116:119], v[168:171], v[64:79]
	ds_read_b128 v[168:171], v193 offset:2048
	v_rcp_f32_e32 v202, v202
	v_mfma_f32_32x32x16_f16 v[80:95], a[116:119], v[172:175], v[80:95]
	ds_read_b128 v[172:175], v193 offset:3072
	global_load_lds_dwordx4 v192, s[44:45] offset:3072 sc1
	v_rcp_f32_e32 v203, v203
	s_waitcnt lgkmcnt(4)
	v_mfma_f32_32x32x16_f16 v[64:79], a[120:123], v[176:179], v[64:79]
	ds_read_b128 v[176:179], v193 offset:4096
	v_rcp_f32_e32 v204, v204
	v_mfma_f32_32x32x16_f16 v[80:95], a[120:123], v[180:183], v[80:95]
	ds_read_b128 v[180:183], v193 offset:5120
	v_rcp_f32_e32 v205, v205
	v_mul_f32_e32 v204, v204, v140
	v_mfma_f32_32x32x2_f32 v[0:15], v248, v228, v[232:247]
	v_mfma_f32_32x32x16_f16 v[64:79], a[124:127], v[184:187], v[64:79]
	ds_read_b128 v[184:187], v193 offset:6144
	v_rcp_f32_e32 v206, v206
	v_mul_f32_e32 v205, v205, v141
	v_mfma_f32_32x32x2_f32 v[16:31], v248, v229, v[232:247]
	v_mfma_f32_32x32x16_f16 v[80:95], a[124:127], v[188:191], v[80:95]
	ds_read_b128 v[188:191], v193 offset:7168
	v_cmp_gt_u32_e32 vcc, 4, v251
	s_cbranch_vccz .LE_tok35

.LE_tok35:
	s_and_b32 s64, s71, 1
	s_lshl_b32 s64, s64, 22
	s_add_u32 s64, s64, s49
	s_add_u32 s64, s64, 0x60000
	s_add_u32 s34, s6, s64
	s_addc_u32 s35, s7, 0
	s_add_u32 s44, s34, 0x0
	s_addc_u32 s45, s35, 0
	s_mov_b32 m0, s52
	s_nop 0
	global_load_lds_dwordx4 v192, s[44:45] sc1
	v_rcp_f32_e32 v207, v207
	v_mul_f32_e32 v206, v206, v142
	s_waitcnt lgkmcnt(4)
	v_mfma_f32_32x32x16_f16 v[64:79], a[128:131], v[160:163], v[64:79]
	ds_read_b128 v[160:163], v193 offset:8192
	v_rcp_f32_e32 v208, v208
	v_mul_f32_e32 v207, v207, v143
	v_mfma_f32_32x32x16_f16 v[80:95], a[128:131], v[164:167], v[80:95]
	ds_read_b128 v[164:167], v193 offset:9216
	v_rcp_f32_e32 v209, v209
	v_fmamk_f32 v208, v208, 0xc0b8aa3b, v198
	v_mfma_f32_32x32x16_f16 v[64:79], a[132:135], v[168:171], v[64:79]
	ds_read_b128 v[168:171], v193 offset:10240
	v_rcp_f32_e32 v210, v210
	v_fmamk_f32 v209, v209, 0xc0b8aa3b, v198
	v_fma_f32 v140, v200, v208, v204
	v_mfma_f32_32x32x16_f16 v[80:95], a[132:135], v[172:175], v[80:95]
	ds_read_b128 v[172:175], v193 offset:11264
	global_load_lds_dwordx4 v192, s[44:45] offset:1024 sc1
	v_rcp_f32_e32 v211, v211
	v_fmamk_f32 v210, v210, 0xc0b8aa3b, v198
	v_fma_f32 v141, v201, v209, v205
	s_waitcnt lgkmcnt(4)
	v_mfma_f32_32x32x16_f16 v[64:79], a[136:139], v[176:179], v[64:79]
	ds_read_b128 v[176:179], v193 offset:12288
	v_rcp_f32_e32 v212, v212
	v_fmamk_f32 v211, v211, 0xc0b8aa3b, v198
	v_fma_f32 v142, v202, v210, v206
	v_mfma_f32_32x32x16_f16 v[80:95], a[136:139], v[180:183], v[80:95]
	ds_read_b128 v[180:183], v193 offset:13312
	v_rcp_f32_e32 v213, v213
	v_fma_f32 v143, v203, v211, v207
	v_mfma_f32_32x32x16_f16 v[64:79], a[140:143], v[184:187], v[64:79]
	ds_read_b128 v[184:187], v193 offset:14336
	v_rcp_f32_e32 v214, v214
	v_mfma_f32_32x32x16_f16 v[80:95], a[140:143], v[188:191], v[80:95]
	ds_read_b128 v[188:191], v193 offset:15360
	global_load_lds_dwordx4 v192, s[44:45] offset:2048 sc1
	v_rcp_f32_e32 v215, v215
	s_waitcnt lgkmcnt(4)
	v_mfma_f32_32x32x16_f16 v[64:79], a[144:147], v[160:163], v[64:79]
	ds_read_b128 v[160:163], v193 offset:16384
	v_exp_f32_e32 v200, v140
	v_mfma_f32_32x32x16_f16 v[80:95], a[144:147], v[164:167], v[80:95]
	ds_read_b128 v[164:167], v193 offset:17408
	v_exp_f32_e32 v201, v141
	v_add_f32_e32 v200, 1.0, v200
	v_mfma_f32_32x32x16_f16 v[64:79], a[148:151], v[168:171], v[64:79]
	ds_read_b128 v[168:171], v193 offset:18432
	v_exp_f32_e32 v202, v142
	v_add_f32_e32 v201, 1.0, v201
	v_mfma_f32_32x32x16_f16 v[80:95], a[148:151], v[172:175], v[80:95]
	ds_read_b128 v[172:175], v193 offset:19456
	global_load_lds_dwordx4 v192, s[44:45] offset:3072 sc1
	v_exp_f32_e32 v203, v143
	v_add_f32_e32 v202, 1.0, v202
	s_waitcnt lgkmcnt(4)
	v_mfma_f32_32x32x16_f16 v[64:79], a[152:155], v[176:179], v[64:79]
	ds_read_b128 v[176:179], v193 offset:20480
	v_add_f32_e32 v203, 1.0, v203
	v_rcp_f32_e32 v200, v200
	v_mfma_f32_32x32x16_f16 v[80:95], a[152:155], v[180:183], v[80:95]
	ds_read_b128 v[180:183], v193 offset:21504
	v_rcp_f32_e32 v201, v201
	v_fma_f32 v200, v200, 2.0, -1.0
	v_mfma_f32_32x32x16_f16 v[64:79], a[156:159], v[184:187], v[64:79]
	ds_read_b128 v[184:187], v193 offset:22528
	v_rcp_f32_e32 v202, v202
	v_fma_f32 v201, v201, 2.0, -1.0
	v_mul_f32_e32 v216, v212, v200
	v_mfma_f32_32x32x16_f16 v[80:95], a[156:159], v[188:191], v[80:95]
	ds_read_b128 v[188:191], v193 offset:23552
	s_add_u32 s44, s34, 0x1000
	s_addc_u32 s45, s35, 0
	s_mov_b32 m0, s53
	s_nop 0
	global_load_lds_dwordx4 v192, s[44:45] sc1
	v_rcp_f32_e32 v203, v203
	v_fma_f32 v202, v202, 2.0, -1.0
	v_mul_f32_e32 v217, v213, v201
	s_waitcnt lgkmcnt(4)
	v_mfma_f32_32x32x16_f16 v[64:79], a[160:163], v[160:163], v[64:79]
	ds_read_b128 v[160:163], v193 offset:24576
	v_fma_f32 v203, v203, 2.0, -1.0
	v_mul_f32_e32 v218, v214, v202
	v_mfma_f32_32x32x16_f16 v[80:95], a[160:163], v[164:167], v[80:95]
	ds_read_b128 v[164:167], v193 offset:25600
	v_mul_f32_e32 v219, v215, v203
	v_cvt_pk_f16_f32 v222, v216, v217
	v_mfma_f32_32x32x16_f16 v[64:79], a[164:167], v[168:171], v[64:79]
	ds_read_b128 v[168:171], v193 offset:26624
	v_cvt_pk_f16_f32 v223, v218, v219
	v_mfma_f32_32x32x16_f16 v[80:95], a[164:167], v[172:175], v[80:95]
	ds_read_b128 v[172:175], v193 offset:27648
	global_load_lds_dwordx4 v192, s[44:45] offset:1024 sc1
	s_cmp_lg_u32 s33, s60
	s_cbranch_scc1 .LE_nht37
	s_add_u32 s46, s62, 0x60000
	s_addc_u32 s47, s63, 0
	global_store_dwordx4 v250, v[216:219], s[46:47]
	s_waitcnt vmcnt(0)

.LE_join41:
	v_mfma_f32_32x32x16_f16 v[64:79], a[196:199], v[168:171], v[64:79]
	ds_read_b128 v[168:171], v193 offset:43008
	v_mfma_f32_32x32x16_f16 v[80:95], a[196:199], v[172:175], v[80:95]
	ds_read_b128 v[172:175], v193 offset:44032
	global_load_lds_dwordx4 v192, s[44:45] offset:1024 sc1
	s_waitcnt lgkmcnt(4)
	v_mfma_f32_32x32x16_f16 v[64:79], a[200:203], v[176:179], v[64:79]
	ds_read_b128 v[176:179], v193 offset:45056
	v_mfma_f32_32x32x16_f16 v[80:95], a[200:203], v[180:183], v[80:95]
	ds_read_b128 v[180:183], v193 offset:46080
	v_mfma_f32_32x32x16_f16 v[64:79], a[204:207], v[184:187], v[64:79]
	ds_read_b128 v[184:187], v193 offset:47104
	v_mfma_f32_32x32x16_f16 v[80:95], a[204:207], v[188:191], v[80:95]
	ds_read_b128 v[188:191], v193 offset:48128
	global_load_lds_dwordx4 v192, s[44:45] offset:2048 sc1
	s_waitcnt lgkmcnt(4)
	v_mfma_f32_32x32x16_f16 v[64:79], a[208:211], v[160:163], v[64:79]
	ds_read_b128 v[160:163], v193 offset:49152
	v_mfma_f32_32x32x16_f16 v[80:95], a[208:211], v[164:167], v[80:95]
	ds_read_b128 v[164:167], v193 offset:50176
	v_mfma_f32_32x32x16_f16 v[64:79], a[212:215], v[168:171], v[64:79]
	ds_read_b128 v[168:171], v193 offset:51200
	v_mfma_f32_32x32x16_f16 v[80:95], a[212:215], v[172:175], v[80:95]
	ds_read_b128 v[172:175], v193 offset:52224
	global_load_lds_dwordx4 v192, s[44:45] offset:3072 sc1
	s_waitcnt lgkmcnt(4)
	v_mfma_f32_32x32x16_f16 v[64:79], a[216:219], v[176:179], v[64:79]
	ds_read_b128 v[176:179], v193 offset:53248
	v_mfma_f32_32x32x16_f16 v[80:95], a[216:219], v[180:183], v[80:95]
	ds_read_b128 v[180:183], v193 offset:54272
	v_mfma_f32_32x32x16_f16 v[64:79], a[220:223], v[184:187], v[64:79]
	ds_read_b128 v[184:187], v193 offset:55296
	v_mfma_f32_32x32x16_f16 v[80:95], a[220:223], v[188:191], v[80:95]
	ds_read_b128 v[188:191], v193 offset:56320
	s_add_u32 s44, s34, 0x9000
	s_addc_u32 s45, s35, 0
	s_mov_b32 m0, s55
	s_nop 0
	global_load_lds_dwordx4 v192, s[44:45] sc1
	s_waitcnt lgkmcnt(4)
	v_mfma_f32_32x32x16_f16 v[64:79], a[224:227], v[160:163], v[64:79]
	ds_read_b128 v[160:163], v193 offset:57344
	v_mfma_f32_32x32x16_f16 v[80:95], a[224:227], v[164:167], v[80:95]
	ds_read_b128 v[164:167], v193 offset:58368
	v_mfma_f32_32x32x16_f16 v[64:79], a[228:231], v[168:171], v[64:79]
	ds_read_b128 v[168:171], v193 offset:59392
	v_mfma_f32_32x32x16_f16 v[80:95], a[228:231], v[172:175], v[80:95]
	ds_read_b128 v[172:175], v193 offset:60416
	global_load_lds_dwordx4 v192, s[44:45] offset:1024 sc1
	s_waitcnt lgkmcnt(4)
	v_mfma_f32_32x32x16_f16 v[64:79], a[232:235], v[176:179], v[64:79]
	ds_read_b128 v[176:179], v193 offset:61440
	v_mfma_f32_32x32x16_f16 v[80:95], a[232:235], v[180:183], v[80:95]
	ds_read_b128 v[180:183], v193 offset:62464
	v_mfma_f32_32x32x16_f16 v[64:79], a[236:239], v[184:187], v[64:79]
	ds_read_b128 v[184:187], v193 offset:63488
	v_mfma_f32_32x32x16_f16 v[80:95], a[236:239], v[188:191], v[80:95]
	ds_read_b128 v[188:191], v193 offset:64512
	global_load_lds_dwordx4 v192, s[44:45] offset:2048 sc1
	s_waitcnt vmcnt(8)
	s_barrier
	s_waitcnt lgkmcnt(4)
	v_mfma_f32_32x32x16_f16 v[64:79], a[240:243], v[160:163], v[64:79]
	ds_read_b128 v[160:163], v192 offset:0
	v_mfma_f32_32x32x16_f16 v[80:95], a[240:243], v[164:167], v[80:95]
	ds_read_b128 v[164:167], v192 offset:1024
	v_mfma_f32_32x32x16_f16 v[64:79], a[244:247], v[168:171], v[64:79]
	ds_read_b128 v[168:171], v192 offset:2048
	v_mfma_f32_32x32x16_f16 v[80:95], a[244:247], v[172:175], v[80:95]
	ds_read_b128 v[172:175], v192 offset:3072
	global_load_lds_dwordx4 v192, s[44:45] offset:3072 sc1
	s_waitcnt lgkmcnt(4)
	v_mfma_f32_32x32x16_f16 v[64:79], a[248:251], v[176:179], v[64:79]
	ds_read_b128 v[176:179], v192 offset:4096
	v_mfma_f32_32x32x16_f16 v[80:95], a[248:251], v[180:183], v[80:95]
	ds_read_b128 v[180:183], v192 offset:5120
	v_mfma_f32_32x32x16_f16 v[64:79], a[252:255], v[184:187], v[64:79]
	ds_read_b128 v[184:187], v192 offset:6144
	v_mfma_f32_32x32x16_f16 v[80:95], a[252:255], v[188:191], v[80:95]
	ds_read_b128 v[188:191], v192 offset:7168
	s_add_u32 s44, s34, 0x10000
	s_addc_u32 s45, s35, 0
	s_mov_b32 m0, s56
	s_nop 0
	global_load_lds_dwordx4 v192, s[44:45] sc1
	s_and_b32 s64, s33, 1
	s_lshl_b32 s64, s64, 22
	s_add_u32 s64, s64, s50
	s_add_u32 s64, s64, 0x40000
	s_add_u32 s36, s6, s64
	s_addc_u32 s37, s7, 0
	s_lshl_b32 s64, s33, 3
	s_add_u32 s64, s64, s29
	s_lshl_b32 s64, s64, 5
	s_add_u32 s64, s64, s30
	s_lshl_b32 s64, s64, 2
	s_add_u32 s40, s8, s64
	s_addc_u32 s41, s9, 0
	s_lshl_b32 s64, s61, 11
	s_lshl_b32 s65, s29, 8
	s_add_u32 s64, s64, s65
	s_add_u32 s64, s64, 64
	s_lshl_b32 s64, s64, 3
	s_add_u32 s42, s12, s64
	s_addc_u32 s43, s13, 0
	s_nop 3
	global_load_dword v228, v249, s[42:43] offset:0
	global_load_dword v229, v249, s[42:43] offset:256
	s_waitcnt lgkmcnt(4)
	v_mfma_f32_32x32x16_f16 v[96:111], a[0:3], v[160:163], v[96:111]
	ds_read_b128 v[160:163], v192 offset:8192
	v_exp_f32_e32 v200, v64
	v_mfma_f32_32x32x16_f16 v[112:127], a[0:3], v[164:167], v[112:127]
	ds_read_b128 v[164:167], v192 offset:9216
	s_lshl_b32 s64, s33, 3
	s_add_u32 s64, s64, s29
	s_lshl_b32 s64, s64, 7
	s_add_u32 s38, s8, s64
	s_addc_u32 s39, s9, 0
	global_load_dword v251, v196, s[38:39] sc1
	v_exp_f32_e32 v201, v65
	v_add_f32_e32 v200, 1.0, v200
	v_mfma_f32_32x32x16_f16 v[96:111], a[4:7], v[168:171], v[96:111]
	ds_read_b128 v[168:171], v192 offset:10240
	v_exp_f32_e32 v202, v66
	v_add_f32_e32 v201, 1.0, v201
	v_mfma_f32_32x32x16_f16 v[112:127], a[4:7], v[172:175], v[112:127]
	ds_read_b128 v[172:175], v192 offset:11264
	global_load_lds_dwordx4 v192, s[44:45] offset:1024 sc1
	v_exp_f32_e32 v203, v67
	v_add_f32_e32 v202, 1.0, v202
	s_waitcnt lgkmcnt(4)
	v_mfma_f32_32x32x16_f16 v[96:111], a[8:11], v[176:179], v[96:111]
	ds_read_b128 v[176:179], v192 offset:12288
	v_exp_f32_e32 v204, v68
	v_add_f32_e32 v203, 1.0, v203
	v_mfma_f32_32x32x16_f16 v[112:127], a[8:11], v[180:183], v[112:127]
	ds_read_b128 v[180:183], v192 offset:13312
	v_exp_f32_e32 v205, v69
	v_add_f32_e32 v204, 1.0, v204
	v_mfma_f32_32x32x16_f16 v[96:111], a[12:15], v[184:187], v[96:111]
	ds_read_b128 v[184:187], v192 offset:14336
	v_exp_f32_e32 v206, v70
	v_add_f32_e32 v205, 1.0, v205
	v_mfma_f32_32x32x16_f16 v[112:127], a[12:15], v[188:191], v[112:127]
	ds_read_b128 v[188:191], v192 offset:15360
	global_load_lds_dwordx4 v192, s[44:45] offset:2048 sc1
	v_exp_f32_e32 v207, v71
	v_add_f32_e32 v206, 1.0, v206
	s_waitcnt lgkmcnt(4)
	v_mfma_f32_32x32x16_f16 v[96:111], a[16:19], v[160:163], v[96:111]
	ds_read_b128 v[160:163], v192 offset:16384
	v_exp_f32_e32 v208, v72
	v_add_f32_e32 v207, 1.0, v207
	v_mfma_f32_32x32x16_f16 v[112:127], a[16:19], v[164:167], v[112:127]
	ds_read_b128 v[164:167], v192 offset:17408
	v_exp_f32_e32 v209, v73
	v_add_f32_e32 v208, 1.0, v208
	v_mfma_f32_32x32x16_f16 v[96:111], a[20:23], v[168:171], v[96:111]
	ds_read_b128 v[168:171], v192 offset:18432
	v_exp_f32_e32 v210, v74
	v_add_f32_e32 v209, 1.0, v209
	v_mfma_f32_32x32x16_f16 v[112:127], a[20:23], v[172:175], v[112:127]
	ds_read_b128 v[172:175], v192 offset:19456
	global_load_lds_dwordx4 v192, s[44:45] offset:3072 sc1
	v_exp_f32_e32 v211, v75
	v_add_f32_e32 v210, 1.0, v210
	s_waitcnt lgkmcnt(4)
	v_mfma_f32_32x32x16_f16 v[96:111], a[24:27], v[176:179], v[96:111]
	ds_read_b128 v[176:179], v192 offset:20480
	v_exp_f32_e32 v212, v76
	v_add_f32_e32 v211, 1.0, v211
	v_mfma_f32_32x32x16_f16 v[112:127], a[24:27], v[180:183], v[112:127]
	ds_read_b128 v[180:183], v192 offset:21504
	v_exp_f32_e32 v213, v77
	v_add_f32_e32 v212, 1.0, v212
	v_mfma_f32_32x32x16_f16 v[96:111], a[28:31], v[184:187], v[96:111]
	ds_read_b128 v[184:187], v192 offset:22528
	v_exp_f32_e32 v214, v78
	v_add_f32_e32 v213, 1.0, v213
	v_mfma_f32_32x32x16_f16 v[112:127], a[28:31], v[188:191], v[112:127]
	ds_read_b128 v[188:191], v192 offset:23552
	s_add_u32 s44, s34, 0x11000
	s_addc_u32 s45, s35, 0
	s_mov_b32 m0, s57
	s_nop 0
	global_load_lds_dwordx4 v192, s[44:45] sc1
	v_exp_f32_e32 v215, v79
	v_add_f32_e32 v214, 1.0, v214
	s_waitcnt lgkmcnt(4)
	v_mfma_f32_32x32x16_f16 v[96:111], a[32:35], v[160:163], v[96:111]
	ds_read_b128 v[160:163], v192 offset:24576
	v_add_f32_e32 v215, 1.0, v215
	v_rcp_f32_e32 v200, v200
	v_mfma_f32_32x32x16_f16 v[112:127], a[32:35], v[164:167], v[112:127]
	ds_read_b128 v[164:167], v192 offset:25600
	v_rcp_f32_e32 v201, v201
	v_mfma_f32_32x32x16_f16 v[96:111], a[36:39], v[168:171], v[96:111]
	ds_read_b128 v[168:171], v192 offset:26624
	v_rcp_f32_e32 v202, v202
	v_mfma_f32_32x32x16_f16 v[112:127], a[36:39], v[172:175], v[112:127]
	ds_read_b128 v[172:175], v192 offset:27648
	global_load_lds_dwordx4 v192, s[44:45] offset:1024 sc1
	v_rcp_f32_e32 v203, v203
	s_waitcnt lgkmcnt(4)
	v_mfma_f32_32x32x16_f16 v[96:111], a[40:43], v[176:179], v[96:111]
	ds_read_b128 v[176:179], v192 offset:28672
	v_rcp_f32_e32 v204, v204
	v_mfma_f32_32x32x16_f16 v[112:127], a[40:43], v[180:183], v[112:127]
	ds_read_b128 v[180:183], v192 offset:29696
	v_rcp_f32_e32 v205, v205
	v_mul_f32_e32 v204, v204, v144
	v_mfma_f32_32x32x16_f16 v[96:111], a[44:47], v[184:187], v[96:111]
	ds_read_b128 v[184:187], v192 offset:30720
	v_rcp_f32_e32 v206, v206
	v_mul_f32_e32 v205, v205, v145
	v_mfma_f32_32x32x16_f16 v[112:127], a[44:47], v[188:191], v[112:127]
	ds_read_b128 v[188:191], v192 offset:31744
	global_load_lds_dwordx4 v192, s[44:45] offset:2048 sc1
	v_rcp_f32_e32 v207, v207
	v_mul_f32_e32 v206, v206, v146
	s_waitcnt vmcnt(10)
	s_barrier
	s_waitcnt lgkmcnt(4)
	v_mfma_f32_32x32x16_f16 v[96:111], a[48:51], v[160:163], v[96:111]
	ds_read_b128 v[160:163], v192 offset:32768
	v_rcp_f32_e32 v208, v208
	v_mul_f32_e32 v207, v207, v147
	v_mfma_f32_32x32x16_f16 v[112:127], a[48:51], v[164:167], v[112:127]
	ds_read_b128 v[164:167], v192 offset:33792
	v_rcp_f32_e32 v209, v209
	v_fmamk_f32 v208, v208, 0xc0b8aa3b, v198
	v_mfma_f32_32x32x16_f16 v[96:111], a[52:55], v[168:171], v[96:111]
	ds_read_b128 v[168:171], v192 offset:34816
	v_rcp_f32_e32 v210, v210
	v_fmamk_f32 v209, v209, 0xc0b8aa3b, v198
	v_fma_f32 v144, v200, v208, v204
	v_mfma_f32_32x32x16_f16 v[112:127], a[52:55], v[172:175], v[112:127]
	ds_read_b128 v[172:175], v192 offset:35840
	global_load_lds_dwordx4 v192, s[44:45] offset:3072 sc1
	v_rcp_f32_e32 v211, v211
	v_fmamk_f32 v210, v210, 0xc0b8aa3b, v198
	v_fma_f32 v145, v201, v209, v205
	s_waitcnt lgkmcnt(4)
	v_mfma_f32_32x32x16_f16 v[96:111], a[56:59], v[176:179], v[96:111]
	ds_read_b128 v[176:179], v192 offset:36864
	v_rcp_f32_e32 v212, v212
	v_fmamk_f32 v211, v211, 0xc0b8aa3b, v198
	v_fma_f32 v146, v202, v210, v206
	v_mfma_f32_32x32x16_f16 v[112:127], a[56:59], v[180:183], v[112:127]
	ds_read_b128 v[180:183], v192 offset:37888
	v_rcp_f32_e32 v213, v213
	v_fma_f32 v147, v203, v211, v207
	v_mfma_f32_32x32x16_f16 v[96:111], a[60:63], v[184:187], v[96:111]
	ds_read_b128 v[184:187], v192 offset:38912
	v_rcp_f32_e32 v214, v214
	v_mfma_f32_32x32x16_f16 v[112:127], a[60:63], v[188:191], v[112:127]
	ds_read_b128 v[188:191], v192 offset:39936
	s_add_u32 s44, s34, 0x18000
	s_addc_u32 s45, s35, 0
	s_mov_b32 m0, s58
	s_nop 0
	global_load_lds_dwordx4 v192, s[44:45] sc1
	v_rcp_f32_e32 v215, v215
	s_waitcnt lgkmcnt(4)
	v_mfma_f32_32x32x16_f16 v[96:111], a[64:67], v[160:163], v[96:111]
	ds_read_b128 v[160:163], v192 offset:40960
	v_exp_f32_e32 v200, v144
	v_mfma_f32_32x32x16_f16 v[112:127], a[64:67], v[164:167], v[112:127]
	ds_read_b128 v[164:167], v192 offset:41984
	v_exp_f32_e32 v201, v145
	v_add_f32_e32 v200, 1.0, v200
	v_mfma_f32_32x32x16_f16 v[96:111], a[68:71], v[168:171], v[96:111]
	ds_read_b128 v[168:171], v192 offset:43008
	v_exp_f32_e32 v202, v146
	v_add_f32_e32 v201, 1.0, v201
	v_mfma_f32_32x32x16_f16 v[112:127], a[68:71], v[172:175], v[112:127]
	ds_read_b128 v[172:175], v192 offset:44032
	global_load_lds_dwordx4 v192, s[44:45] offset:1024 sc1
	v_exp_f32_e32 v203, v147
	v_add_f32_e32 v202, 1.0, v202
	s_waitcnt lgkmcnt(4)
	v_mfma_f32_32x32x16_f16 v[96:111], a[72:75], v[176:179], v[96:111]
	ds_read_b128 v[176:179], v192 offset:45056
	v_add_f32_e32 v203, 1.0, v203
	v_rcp_f32_e32 v200, v200
	v_mfma_f32_32x32x16_f16 v[112:127], a[72:75], v[180:183], v[112:127]
	ds_read_b128 v[180:183], v192 offset:46080
	v_rcp_f32_e32 v201, v201
	v_fma_f32 v200, v200, 2.0, -1.0
	v_mfma_f32_32x32x16_f16 v[96:111], a[76:79], v[184:187], v[96:111]
	ds_read_b128 v[184:187], v192 offset:47104
	v_rcp_f32_e32 v202, v202
	v_fma_f32 v201, v201, 2.0, -1.0
	v_mul_f32_e32 v216, v212, v200
	v_mfma_f32_32x32x16_f16 v[112:127], a[76:79], v[188:191], v[112:127]
	ds_read_b128 v[188:191], v192 offset:48128
	global_load_lds_dwordx4 v192, s[44:45] offset:2048 sc1
	v_rcp_f32_e32 v203, v203
	v_fma_f32 v202, v202, 2.0, -1.0
	v_mul_f32_e32 v217, v213, v201
	s_waitcnt lgkmcnt(4)
	v_mfma_f32_32x32x16_f16 v[96:111], a[80:83], v[160:163], v[96:111]
	ds_read_b128 v[160:163], v192 offset:49152
	v_fma_f32 v203, v203, 2.0, -1.0
	v_mul_f32_e32 v218, v214, v202
	v_exp_f32_e32 v200, v80
	v_mfma_f32_32x32x16_f16 v[112:127], a[80:83], v[164:167], v[112:127]
	ds_read_b128 v[164:167], v192 offset:50176
	v_mul_f32_e32 v219, v215, v203
	v_cvt_pk_f16_f32 v220, v216, v217
	v_exp_f32_e32 v201, v81
	v_mfma_f32_32x32x16_f16 v[96:111], a[84:87], v[168:171], v[96:111]
	ds_read_b128 v[168:171], v192 offset:51200
	v_cvt_pk_f16_f32 v221, v218, v219
	v_exp_f32_e32 v202, v82
	v_add_f32_e32 v200, 1.0, v200
	v_mfma_f32_32x32x16_f16 v[112:127], a[84:87], v[172:175], v[112:127]
	ds_read_b128 v[172:175], v192 offset:52224
	global_load_lds_dwordx4 v192, s[44:45] offset:3072 sc1
	s_cmp_lg_u32 s33, s60
	s_cbranch_scc1 .LE_nht42
	s_add_u32 s46, s62, 0x80000
	s_addc_u32 s47, s63, 0
	global_store_dwordx4 v250, v[216:219], s[46:47]
	s_waitcnt vmcnt(0)
.LE_nht42:
	v_exp_f32_e32 v203, v83
	s_waitcnt lgkmcnt(4)
	v_mfma_f32_32x32x16_f16 v[96:111], a[88:91], v[176:179], v[96:111]
	ds_read_b128 v[176:179], v192 offset:53248
	v_exp_f32_e32 v204, v84
	v_add_f32_e32 v201, 1.0, v201
	v_add_f32_e32 v202, 1.0, v202
	v_mfma_f32_32x32x16_f16 v[112:127], a[88:91], v[180:183], v[112:127]
	ds_read_b128 v[180:183], v192 offset:54272
	v_exp_f32_e32 v205, v85
	v_add_f32_e32 v203, 1.0, v203
	v_add_f32_e32 v204, 1.0, v204
	v_mfma_f32_32x32x16_f16 v[96:111], a[92:95], v[184:187], v[96:111]
	ds_read_b128 v[184:187], v192 offset:55296
	v_exp_f32_e32 v206, v86
	v_add_f32_e32 v205, 1.0, v205
	v_mfma_f32_32x32x16_f16 v[112:127], a[92:95], v[188:191], v[112:127]
	ds_read_b128 v[188:191], v192 offset:56320
	s_add_u32 s44, s34, 0x19000
	s_addc_u32 s45, s35, 0
	s_mov_b32 m0, s59
	s_nop 0
	global_load_lds_dwordx4 v192, s[44:45] sc1
	v_exp_f32_e32 v207, v87
	v_add_f32_e32 v206, 1.0, v206
	s_waitcnt lgkmcnt(4)
	v_mfma_f32_32x32x16_f16 v[96:111], a[96:99], v[160:163], v[96:111]
	ds_read_b128 v[160:163], v192 offset:57344
	v_exp_f32_e32 v208, v88
	v_add_f32_e32 v207, 1.0, v207
	v_mfma_f32_32x32x16_f16 v[112:127], a[96:99], v[164:167], v[112:127]
	ds_read_b128 v[164:167], v192 offset:58368
	v_exp_f32_e32 v209, v89
	v_add_f32_e32 v208, 1.0, v208
	v_mfma_f32_32x32x16_f16 v[96:111], a[100:103], v[168:171], v[96:111]
	ds_read_b128 v[168:171], v192 offset:59392
	v_exp_f32_e32 v210, v90
	v_add_f32_e32 v209, 1.0, v209
	v_mfma_f32_32x32x16_f16 v[112:127], a[100:103], v[172:175], v[112:127]
	ds_read_b128 v[172:175], v192 offset:60416
	global_load_lds_dwordx4 v192, s[44:45] offset:1024 sc1
	v_exp_f32_e32 v211, v91
	v_add_f32_e32 v210, 1.0, v210
	s_waitcnt lgkmcnt(4)
	v_mfma_f32_32x32x16_f16 v[96:111], a[104:107], v[176:179], v[96:111]
	ds_read_b128 v[176:179], v192 offset:61440
	v_exp_f32_e32 v212, v92
	v_add_f32_e32 v211, 1.0, v211
	v_mfma_f32_32x32x16_f16 v[112:127], a[104:107], v[180:183], v[112:127]
	ds_read_b128 v[180:183], v192 offset:62464
	v_exp_f32_e32 v213, v93
	v_add_f32_e32 v212, 1.0, v212
	v_mfma_f32_32x32x16_f16 v[96:111], a[108:111], v[184:187], v[96:111]
	ds_read_b128 v[184:187], v192 offset:63488
	v_exp_f32_e32 v214, v94
	v_add_f32_e32 v213, 1.0, v213
	v_mfma_f32_32x32x16_f16 v[112:127], a[108:111], v[188:191], v[112:127]
	ds_read_b128 v[188:191], v192 offset:64512
	global_load_lds_dwordx4 v192, s[44:45] offset:2048 sc1
	v_exp_f32_e32 v215, v95
	v_add_f32_e32 v214, 1.0, v214
	s_waitcnt vmcnt(7)
	s_barrier
	s_waitcnt lgkmcnt(4)
	v_mfma_f32_32x32x16_f16 v[96:111], a[112:115], v[160:163], v[96:111]
	ds_read_b128 v[160:163], v193 offset:0
	v_add_f32_e32 v215, 1.0, v215
	v_rcp_f32_e32 v200, v200
	v_mfma_f32_32x32x16_f16 v[112:127], a[112:115], v[164:167], v[112:127]
	ds_read_b128 v[164:167], v193 offset:1024
	v_rcp_f32_e32 v201, v201
	v_mfma_f32_32x32x16_f16 v[96:111], a[116:119], v[168:171], v[96:111]
	ds_read_b128 v[168:171], v193 offset:2048
	v_rcp_f32_e32 v202, v202
	v_mfma_f32_32x32x16_f16 v[112:127], a[116:119], v[172:175], v[112:127]
	ds_read_b128 v[172:175], v193 offset:3072
	global_load_lds_dwordx4 v192, s[44:45] offset:3072 sc1
	v_rcp_f32_e32 v203, v203
	s_waitcnt lgkmcnt(4)
	v_mfma_f32_32x32x16_f16 v[96:111], a[120:123], v[176:179], v[96:111]
	ds_read_b128 v[176:179], v193 offset:4096
	v_rcp_f32_e32 v204, v204
	v_mfma_f32_32x32x16_f16 v[112:127], a[120:123], v[180:183], v[112:127]
	ds_read_b128 v[180:183], v193 offset:5120
	v_rcp_f32_e32 v205, v205
	v_mul_f32_e32 v204, v204, v148
	v_mfma_f32_32x32x2_f32 v[32:47], v248, v228, v[232:247]
	v_mfma_f32_32x32x16_f16 v[96:111], a[124:127], v[184:187], v[96:111]
	ds_read_b128 v[184:187], v193 offset:6144
	v_rcp_f32_e32 v206, v206
	v_mul_f32_e32 v205, v205, v149
	v_mfma_f32_32x32x2_f32 v[48:63], v248, v229, v[232:247]
	v_mfma_f32_32x32x16_f16 v[112:127], a[124:127], v[188:191], v[112:127]
	ds_read_b128 v[188:191], v193 offset:7168
	v_cmp_gt_u32_e32 vcc, 1, v251
	s_cbranch_vccz .LE_tok43

.LE_tok43:
	s_and_b32 s64, s33, 1
	s_lshl_b32 s64, s64, 22
	s_add_u32 s64, s64, s49
	s_add_u32 s34, s6, s64
	s_addc_u32 s35, s7, 0
	s_add_u32 s44, s34, 0x0
	s_addc_u32 s45, s35, 0
	s_mov_b32 m0, s52
	s_nop 0
	global_load_lds_dwordx4 v192, s[44:45] sc1
	v_rcp_f32_e32 v207, v207
	v_mul_f32_e32 v206, v206, v150
	s_waitcnt lgkmcnt(4)
	v_mfma_f32_32x32x16_f16 v[96:111], a[128:131], v[160:163], v[96:111]
	ds_read_b128 v[160:163], v193 offset:8192
	v_rcp_f32_e32 v208, v208
	v_mul_f32_e32 v207, v207, v151
	v_mfma_f32_32x32x16_f16 v[112:127], a[128:131], v[164:167], v[112:127]
	ds_read_b128 v[164:167], v193 offset:9216
	v_rcp_f32_e32 v209, v209
	v_fmamk_f32 v208, v208, 0xc0b8aa3b, v198
	v_mfma_f32_32x32x16_f16 v[96:111], a[132:135], v[168:171], v[96:111]
	ds_read_b128 v[168:171], v193 offset:10240
	v_rcp_f32_e32 v210, v210
	v_fmamk_f32 v209, v209, 0xc0b8aa3b, v198
	v_fma_f32 v148, v200, v208, v204
	v_mfma_f32_32x32x16_f16 v[112:127], a[132:135], v[172:175], v[112:127]
	ds_read_b128 v[172:175], v193 offset:11264
	global_load_lds_dwordx4 v192, s[44:45] offset:1024 sc1
	v_rcp_f32_e32 v211, v211
	v_fmamk_f32 v210, v210, 0xc0b8aa3b, v198
	v_fma_f32 v149, v201, v209, v205
	s_waitcnt lgkmcnt(4)
	v_mfma_f32_32x32x16_f16 v[96:111], a[136:139], v[176:179], v[96:111]
	ds_read_b128 v[176:179], v193 offset:12288
	v_rcp_f32_e32 v212, v212
	v_fmamk_f32 v211, v211, 0xc0b8aa3b, v198
	v_fma_f32 v150, v202, v210, v206
	v_mfma_f32_32x32x16_f16 v[112:127], a[136:139], v[180:183], v[112:127]
	ds_read_b128 v[180:183], v193 offset:13312
	v_rcp_f32_e32 v213, v213
	v_fma_f32 v151, v203, v211, v207
	v_mfma_f32_32x32x16_f16 v[96:111], a[140:143], v[184:187], v[96:111]
	ds_read_b128 v[184:187], v193 offset:14336
	v_rcp_f32_e32 v214, v214
	v_mfma_f32_32x32x16_f16 v[112:127], a[140:143], v[188:191], v[112:127]
	ds_read_b128 v[188:191], v193 offset:15360
	global_load_lds_dwordx4 v192, s[44:45] offset:2048 sc1
	v_rcp_f32_e32 v215, v215
	s_waitcnt lgkmcnt(4)
	v_mfma_f32_32x32x16_f16 v[96:111], a[144:147], v[160:163], v[96:111]
	ds_read_b128 v[160:163], v193 offset:16384
	v_exp_f32_e32 v200, v148
	v_mfma_f32_32x32x16_f16 v[112:127], a[144:147], v[164:167], v[112:127]
	ds_read_b128 v[164:167], v193 offset:17408
	v_exp_f32_e32 v201, v149
	v_add_f32_e32 v200, 1.0, v200
	v_mfma_f32_32x32x16_f16 v[96:111], a[148:151], v[168:171], v[96:111]
	ds_read_b128 v[168:171], v193 offset:18432
	v_exp_f32_e32 v202, v150
	v_add_f32_e32 v201, 1.0, v201
	v_mfma_f32_32x32x16_f16 v[112:127], a[148:151], v[172:175], v[112:127]
	ds_read_b128 v[172:175], v193 offset:19456
	global_load_lds_dwordx4 v192, s[44:45] offset:3072 sc1
	v_exp_f32_e32 v203, v151
	v_add_f32_e32 v202, 1.0, v202
	s_waitcnt lgkmcnt(4)
	v_mfma_f32_32x32x16_f16 v[96:111], a[152:155], v[176:179], v[96:111]
	ds_read_b128 v[176:179], v193 offset:20480
	v_add_f32_e32 v203, 1.0, v203
	v_rcp_f32_e32 v200, v200
	v_mfma_f32_32x32x16_f16 v[112:127], a[152:155], v[180:183], v[112:127]
	ds_read_b128 v[180:183], v193 offset:21504
	v_rcp_f32_e32 v201, v201
	v_fma_f32 v200, v200, 2.0, -1.0
	v_mfma_f32_32x32x16_f16 v[96:111], a[156:159], v[184:187], v[96:111]
	ds_read_b128 v[184:187], v193 offset:22528
	v_rcp_f32_e32 v202, v202
	v_fma_f32 v201, v201, 2.0, -1.0
	v_mul_f32_e32 v216, v212, v200
	v_mfma_f32_32x32x16_f16 v[112:127], a[156:159], v[188:191], v[112:127]
	ds_read_b128 v[188:191], v193 offset:23552
	s_add_u32 s44, s34, 0x1000
	s_addc_u32 s45, s35, 0
	s_mov_b32 m0, s53
	s_nop 0
	global_load_lds_dwordx4 v192, s[44:45] sc1
	v_rcp_f32_e32 v203, v203
	v_fma_f32 v202, v202, 2.0, -1.0
	v_mul_f32_e32 v217, v213, v201
	s_waitcnt lgkmcnt(4)
	v_mfma_f32_32x32x16_f16 v[96:111], a[160:163], v[160:163], v[96:111]
	ds_read_b128 v[160:163], v193 offset:24576
	v_fma_f32 v203, v203, 2.0, -1.0
	v_mul_f32_e32 v218, v214, v202
	v_mfma_f32_32x32x16_f16 v[112:127], a[160:163], v[164:167], v[112:127]
	ds_read_b128 v[164:167], v193 offset:25600
	v_mul_f32_e32 v219, v215, v203
	v_cvt_pk_f16_f32 v222, v216, v217
	v_mfma_f32_32x32x16_f16 v[96:111], a[164:167], v[168:171], v[96:111]
	ds_read_b128 v[168:171], v193 offset:26624
	v_cvt_pk_f16_f32 v223, v218, v219
	v_mfma_f32_32x32x16_f16 v[112:127], a[164:167], v[172:175], v[112:127]
	ds_read_b128 v[172:175], v193 offset:27648
	global_load_lds_dwordx4 v192, s[44:45] offset:1024 sc1
	s_cmp_lg_u32 s33, s60
	s_cbranch_scc1 .LE_nht45
	s_add_u32 s46, s62, 0xa0000
	s_addc_u32 s47, s63, 0
	global_store_dwordx4 v250, v[216:219], s[46:47]
	s_waitcnt vmcnt(0)
